# weight-conversion items re-tiled 64k x 256n -> 128k x 128n (same item count): bf16 output written as 256 B per row instead of 128 B
# speedup vs baseline: 1.0019x; 1.0019x over previous
.LBB0_218:
	v_add_u32_e32 v2, 0x800, v130
	s_lshr_b32 s0, s12, 7
	v_ashrrev_i32_e32 v41, 5, v2
	v_cvt_f32_u32_e32 v2, s0
	s_sub_i32 s13, 0, s0
	s_abs_i32 s9, s14
	s_ashr_i32 s8, s14, 31
	v_rcp_iflag_f32_e32 v2, v2
	v_add_u32_e32 v3, 0xa00, v130
	v_ashrrev_i32_e32 v42, 5, v3
	v_add_u32_e32 v3, 0xc00, v130
	v_mul_f32_e32 v2, 0x4f7ffffe, v2
	v_cvt_u32_f32_e32 v2, v2
	v_lshlrev_b32_e32 v1, 2, v130
	v_ashrrev_i32_e32 v43, 5, v3
	v_add_u32_e32 v3, 0xe00, v130
	v_readfirstlane_b32 s15, v2
	s_mul_i32 s13, s13, s15
	s_mul_hi_u32 s13, s15, s13
	s_add_i32 s15, s15, s13
	s_mul_hi_u32 s13, s9, s15
	s_mul_i32 s15, s13, s0
	s_sub_i32 s9, s9, s15
	s_add_i32 s15, s13, 1
	s_sub_i32 s16, s9, s0
	s_cmp_ge_u32 s9, s0
	s_cselect_b32 s13, s15, s13
	s_cselect_b32 s9, s16, s9
	s_add_i32 s15, s13, 1
	s_cmp_ge_u32 s9, s0
	s_cselect_b32 s9, s15, s13
	s_xor_b32 s9, s9, s8
	s_sub_i32 s13, s9, s8
	s_mul_i32 s0, s13, s0
	s_sub_i32 s0, s14, s0
	s_lshl_b32 s8, s0, 7
	s_ashr_i32 s9, s8, 31
	s_lshl_b64 s[14:15], s[8:9], 2
	s_add_u32 s10, s10, s14
	v_and_b32_e32 v36, 0x7c, v1
	v_ashrrev_i32_e32 v44, 5, v3
	s_addc_u32 s11, s11, s15
	s_lshl_b32 s16, s13, 7
	v_mov_b32_e32 v35, 0
	v_lshlrev_b32_e32 v34, 2, v36
	v_add_u32_e32 v4, s16, v44
	v_lshl_add_u64 v[2:3], s[10:11], 0, v[34:35]
	v_ashrrev_i32_e32 v7, 31, v4
	v_mad_u64_u32 v[4:5], s[10:11], v4, s12, 0
	v_mov_b32_e32 v6, v5
	v_mad_u64_u32 v[6:7], s[10:11], v7, s12, v[6:7]
	v_mov_b32_e32 v5, v6
	v_add_u32_e32 v6, s16, v43
	v_ashrrev_i32_e32 v9, 31, v6
	v_mad_u64_u32 v[6:7], s[10:11], v6, s12, 0
	v_mov_b32_e32 v8, v7
	v_mad_u64_u32 v[8:9], s[10:11], v9, s12, v[8:9]
	v_lshl_add_u64 v[4:5], v[4:5], 2, v[2:3]
	v_mov_b32_e32 v7, v8
	v_lshl_add_u64 v[6:7], v[6:7], 2, v[2:3]
	global_load_dwordx4 v[30:33], v[4:5], off
	global_load_dwordx4 v[26:29], v[6:7], off
	v_add_u32_e32 v4, s16, v42
	v_ashrrev_i32_e32 v7, 31, v4
	v_mad_u64_u32 v[4:5], s[10:11], v4, s12, 0
	v_mov_b32_e32 v6, v5
	v_mad_u64_u32 v[6:7], s[10:11], v7, s12, v[6:7]
	v_mov_b32_e32 v5, v6
	v_add_u32_e32 v6, s16, v41
	v_ashrrev_i32_e32 v9, 31, v6
	v_mad_u64_u32 v[6:7], s[10:11], v6, s12, 0
	v_mov_b32_e32 v8, v7
	v_add_u32_e32 v54, 0x600, v130
	v_mad_u64_u32 v[8:9], s[10:11], v9, s12, v[8:9]
	v_ashrrev_i32_e32 v40, 5, v54
	v_lshl_add_u64 v[4:5], v[4:5], 2, v[2:3]
	v_mov_b32_e32 v7, v8
	v_lshl_add_u64 v[6:7], v[6:7], 2, v[2:3]
	global_load_dwordx4 v[22:25], v[4:5], off
	global_load_dwordx4 v[18:21], v[6:7], off
	v_add_u32_e32 v4, s16, v40
	v_ashrrev_i32_e32 v7, 31, v4
	v_mad_u64_u32 v[4:5], s[10:11], v4, s12, 0
	v_add_u32_e32 v51, 0x400, v130
	v_mov_b32_e32 v6, v5
	v_ashrrev_i32_e32 v39, 5, v51
	v_mad_u64_u32 v[6:7], s[10:11], v7, s12, v[6:7]
	v_mov_b32_e32 v5, v6
	v_add_u32_e32 v6, s16, v39
	v_ashrrev_i32_e32 v9, 31, v6
	v_mad_u64_u32 v[6:7], s[10:11], v6, s12, 0
	v_mov_b32_e32 v8, v7
	v_add_u32_e32 v37, 0x200, v130
	v_mad_u64_u32 v[8:9], s[10:11], v9, s12, v[8:9]
	v_ashrrev_i32_e32 v38, 5, v37
	v_lshl_add_u64 v[4:5], v[4:5], 2, v[2:3]
	v_mov_b32_e32 v7, v8
	v_lshl_add_u64 v[6:7], v[6:7], 2, v[2:3]
	global_load_dwordx4 v[14:17], v[4:5], off
	global_load_dwordx4 v[10:13], v[6:7], off
	v_add_u32_e32 v4, s16, v38
	v_ashrrev_i32_e32 v7, 31, v4
	v_mad_u64_u32 v[4:5], s[10:11], v4, s12, 0
	v_mov_b32_e32 v6, v5
	v_ashrrev_i32_e32 v1, 5, v130
	v_mad_u64_u32 v[6:7], s[10:11], v7, s12, v[6:7]
	v_mov_b32_e32 v5, v6
	v_add_u32_e32 v6, s16, v1
	v_ashrrev_i32_e32 v9, 31, v6
	v_mad_u64_u32 v[6:7], s[10:11], v6, s12, 0
	v_mov_b32_e32 v8, v7
	v_mad_u64_u32 v[8:9], s[10:11], v9, s12, v[8:9]
	v_mov_b32_e32 v7, v8
	v_lshl_add_u64 v[4:5], v[4:5], 2, v[2:3]
	v_lshl_add_u64 v[2:3], v[6:7], 2, v[2:3]
	global_load_dwordx4 v[6:9], v[4:5], off
	s_nop 0
	global_load_dwordx4 v[2:5], v[2:3], off
	v_lshlrev_b32_e32 v45, 3, v130
	v_and_b32_e32 v66, 0x78, v45
	s_movk_i32 s0, 0x204
	v_mad_u32_u24 v55, v66, s0, 0
	v_mul_lo_u32 v57, v1, s0
	v_mul_lo_u32 v58, v38, s0
	v_mul_lo_u32 v59, v39, s0
	v_mul_lo_u32 v60, v40, s0
	v_mul_lo_u32 v61, v41, s0
	v_mul_lo_u32 v62, v42, s0
	v_mul_lo_u32 v63, v43, s0
	v_mul_lo_u32 v64, v44, s0
	s_add_u32 s0, s6, 0x1e940000
	s_addc_u32 s9, s7, 0
	s_add_u32 s12, s6, 0x16940000
	s_addc_u32 s13, s7, 0
	s_add_u32 s14, s6, 0x16140000
	s_addc_u32 s15, s7, 0
	s_add_u32 s30, s6, 0x15540000
	s_addc_u32 s31, s7, 0
	s_add_u32 s6, s6, 0x11f40000
	v_add_u32_e32 v34, 0, v34
	v_ashrrev_i32_e32 v45, 4, v130
	v_ashrrev_i32_e32 v48, 4, v37
	v_ashrrev_i32_e32 v51, 4, v51
	v_ashrrev_i32_e32 v54, 4, v54
	s_addc_u32 s7, s7, 0
	s_add_i32 s10, s33, s38
	s_mov_b32 s11, 0
	v_lshl_add_u32 v46, v45, 2, v55
	v_and_b32_e32 v47, 15, v45
	v_lshl_add_u32 v49, v48, 2, v55
	v_and_b32_e32 v50, 15, v48
	v_lshl_add_u32 v52, v51, 2, v55
	v_and_b32_e32 v53, 15, v51
	v_lshl_add_u32 v55, v54, 2, v55
	v_and_b32_e32 v56, 15, v54
	s_add_i32 s34, s10, 0xfffff5c0
	s_add_i32 s35, s10, 0xfffff6c0
	v_add_u32_e32 v57, v34, v57
	v_add_u32_e32 v58, v34, v58
	v_add_u32_e32 v59, v34, v59
	v_add_u32_e32 v60, v34, v60
	v_add_u32_e32 v61, v34, v61
	v_add_u32_e32 v62, v34, v62
	v_add_u32_e32 v63, v34, v63
	v_add_u32_e32 v64, v34, v64
	v_lshlrev_b32_e32 v34, 2, v36
	v_lshlrev_b32_e32 v36, 1, v66
	s_movk_i32 s36, 0x7fff
	v_mov_b32_e32 v65, 1
	s_mov_b32 s26, s17
	s_mov_b32 s27, s29
	s_mov_b64 s[20:21], s[2:3]
	s_branch .LBB0_222

.LBB0_220:
	s_lshr_b32 s22, s39, 7
	v_cvt_f32_u32_e32 v2, s22
	s_sub_i32 s41, 0, s22
	s_abs_i32 s23, s40
	s_ashr_i32 s10, s40, 31
	v_rcp_iflag_f32_e32 v2, v2
	s_nop 0
	v_mul_f32_e32 v2, 0x4f7ffffe, v2
	v_cvt_u32_f32_e32 v2, v2
	s_nop 0
	v_readfirstlane_b32 s42, v2
	s_mul_i32 s41, s41, s42
	s_mul_hi_u32 s41, s42, s41
	s_add_i32 s42, s42, s41
	s_mul_hi_u32 s41, s23, s42
	s_mul_i32 s42, s41, s22
	s_sub_i32 s23, s23, s42
	s_add_i32 s43, s41, 1
	s_sub_i32 s42, s23, s22
	s_cmp_ge_u32 s23, s22
	s_cselect_b32 s41, s43, s41
	s_cselect_b32 s23, s42, s23
	s_add_i32 s42, s41, 1
	s_cmp_ge_u32 s23, s22
	s_cselect_b32 s23, s42, s41
	s_xor_b32 s23, s23, s10
	s_sub_i32 s23, s23, s10
	s_lshl_b32 s10, s23, 7
	s_mul_i32 s23, s23, s22
	s_sub_i32 s22, s40, s23
	s_lshl_b32 s22, s22, 7
	s_ashr_i32 s23, s22, 31
	s_lshl_b64 s[40:41], s[22:23], 2
	s_add_u32 s24, s24, s40
	v_add_u32_e32 v2, s10, v1
	s_addc_u32 s25, s25, s41
	v_add_u32_e32 v10, s10, v39
	v_add_u32_e32 v18, s10, v41
	v_add_u32_e32 v28, s10, v43
	v_ashrrev_i32_e32 v5, 31, v2
	v_lshl_add_u64 v[26:27], s[24:25], 0, v[34:35]
	v_mad_u64_u32 v[2:3], s[24:25], v2, s39, 0
	v_ashrrev_i32_e32 v13, 31, v10
	v_mad_u64_u32 v[10:11], s[24:25], v10, s39, 0
	v_ashrrev_i32_e32 v21, 31, v18
	v_mad_u64_u32 v[18:19], s[24:25], v18, s39, 0
	v_ashrrev_i32_e32 v31, 31, v28
	v_mad_u64_u32 v[28:29], s[24:25], v28, s39, 0
	v_mov_b32_e32 v4, v3
	v_mov_b32_e32 v12, v11
	v_mov_b32_e32 v20, v19
	v_mov_b32_e32 v30, v29
	v_mad_u64_u32 v[4:5], s[24:25], v5, s39, v[4:5]
	v_mad_u64_u32 v[12:13], s[24:25], v13, s39, v[12:13]
	v_mad_u64_u32 v[20:21], s[24:25], v21, s39, v[20:21]
	v_mad_u64_u32 v[30:31], s[24:25], v31, s39, v[30:31]
	v_mov_b32_e32 v3, v4
	v_add_u32_e32 v4, s10, v38
	v_mov_b32_e32 v11, v12
	v_add_u32_e32 v12, s10, v40
	v_mov_b32_e32 v19, v20
	v_add_u32_e32 v20, s10, v42
	v_mov_b32_e32 v29, v30
	v_add_u32_e32 v30, s10, v44
	v_ashrrev_i32_e32 v7, 31, v4
	v_mad_u64_u32 v[4:5], s[24:25], v4, s39, 0
	v_ashrrev_i32_e32 v15, 31, v12
	v_mad_u64_u32 v[12:13], s[24:25], v12, s39, 0
	v_ashrrev_i32_e32 v23, 31, v20
	v_mad_u64_u32 v[20:21], s[24:25], v20, s39, 0
	v_ashrrev_i32_e32 v33, 31, v30
	v_mad_u64_u32 v[30:31], s[24:25], v30, s39, 0
	v_mov_b32_e32 v6, v5
	v_mov_b32_e32 v14, v13
	v_mov_b32_e32 v22, v21
	v_mov_b32_e32 v32, v31
	v_mad_u64_u32 v[6:7], s[24:25], v7, s39, v[6:7]
	v_mad_u64_u32 v[14:15], s[24:25], v15, s39, v[14:15]
	v_mad_u64_u32 v[22:23], s[24:25], v23, s39, v[22:23]
	v_mad_u64_u32 v[32:33], s[24:25], v33, s39, v[32:33]
	v_mov_b32_e32 v5, v6
	v_mov_b32_e32 v13, v14
	v_mov_b32_e32 v21, v22
	v_mov_b32_e32 v31, v32
	v_lshl_add_u64 v[2:3], v[2:3], 2, v[26:27]
	v_lshl_add_u64 v[6:7], v[4:5], 2, v[26:27]
	v_lshl_add_u64 v[10:11], v[10:11], 2, v[26:27]
	v_lshl_add_u64 v[14:15], v[12:13], 2, v[26:27]
	v_lshl_add_u64 v[18:19], v[18:19], 2, v[26:27]
	v_lshl_add_u64 v[22:23], v[20:21], 2, v[26:27]
	v_lshl_add_u64 v[28:29], v[28:29], 2, v[26:27]
	v_lshl_add_u64 v[30:31], v[30:31], 2, v[26:27]
	global_load_dwordx4 v[2:5], v[2:3], off
	s_nop 0
	global_load_dwordx4 v[6:9], v[6:7], off
	s_nop 0
	global_load_dwordx4 v[10:13], v[10:11], off
	s_nop 0
	global_load_dwordx4 v[14:17], v[14:15], off
	s_nop 0
	global_load_dwordx4 v[18:21], v[18:19], off
	s_nop 0
	global_load_dwordx4 v[22:25], v[22:23], off
	s_nop 0
	global_load_dwordx4 v[26:29], v[28:29], off
	s_nop 0
	global_load_dwordx4 v[30:33], v[30:31], off
.LBB0_221:
	s_add_i32 s28, s28, -1
	s_cmp_eq_u32 s17, 0
	v_add_u32_e32 v66, s8, v45
	v_lshlrev_b32_e32 v37, 1, v66
	s_cselect_b64 vcc, -1, 0
	s_ashr_i32 s17, s16, 31
	v_and_b32_e32 v37, 0xffffffe0, v37
	s_lshl_b64 s[16:17], s[16:17], 1
	v_add3_u32 v67, s1, v47, v37
	s_add_u32 s2, s2, s16
	s_addc_u32 s3, s3, s17
	v_mov_b32_e32 v37, v35
	v_cndmask_b32_e32 v66, v67, v66, vcc
	v_lshl_add_u64 v[70:71], s[2:3], 0, v[36:37]
	v_ashrrev_i32_e32 v69, 31, v66
	v_mad_u64_u32 v[66:67], s[2:3], v66, s29, 0
	v_mov_b32_e32 v68, v67
	ds_read_b32 v37, v46
	ds_read_b32 v74, v46 offset:516
	ds_read_b32 v75, v46 offset:1032
	ds_read_b32 v76, v46 offset:1548
	ds_read_b32 v77, v46 offset:2064
	ds_read_b32 v78, v46 offset:2580
	ds_read_b32 v79, v46 offset:3096
	ds_read_b32 v80, v46 offset:3612
	v_mad_u64_u32 v[68:69], s[2:3], v69, s29, v[68:69]
	v_mov_b32_e32 v67, v68
	v_lshl_add_u64 v[72:73], v[66:67], 1, v[70:71]
	s_waitcnt lgkmcnt(7)
	v_and_b32_sdwa v67, v37, v65 dst_sel:DWORD dst_unused:UNUSED_PAD src0_sel:WORD_1 src1_sel:DWORD
	v_add3_u32 v37, v37, v67, s36
	s_waitcnt lgkmcnt(4)
	v_and_b32_sdwa v67, v76, v65 dst_sel:DWORD dst_unused:UNUSED_PAD src0_sel:WORD_1 src1_sel:DWORD
	v_and_b32_sdwa v68, v74, v65 dst_sel:DWORD dst_unused:UNUSED_PAD src0_sel:WORD_1 src1_sel:DWORD
	v_and_b32_sdwa v66, v75, v65 dst_sel:DWORD dst_unused:UNUSED_PAD src0_sel:WORD_1 src1_sel:DWORD
	v_add3_u32 v67, v76, v67, s36
	v_add3_u32 v68, v74, v68, s36
	v_add3_u32 v66, v75, v66, s36
	v_and_b32_e32 v67, 0xffff0000, v67
	v_and_b32_e32 v68, 0xffff0000, v68
	s_waitcnt lgkmcnt(0)
	v_and_b32_sdwa v69, v80, v65 dst_sel:DWORD dst_unused:UNUSED_PAD src0_sel:WORD_1 src1_sel:DWORD
	v_and_b32_sdwa v74, v78, v65 dst_sel:DWORD dst_unused:UNUSED_PAD src0_sel:WORD_1 src1_sel:DWORD
	v_or_b32_sdwa v67, v67, v66 dst_sel:DWORD dst_unused:UNUSED_PAD src0_sel:DWORD src1_sel:WORD_1
	v_or_b32_sdwa v66, v68, v37 dst_sel:DWORD dst_unused:UNUSED_PAD src0_sel:DWORD src1_sel:WORD_1
	v_and_b32_sdwa v37, v79, v65 dst_sel:DWORD dst_unused:UNUSED_PAD src0_sel:WORD_1 src1_sel:DWORD
	v_and_b32_sdwa v68, v77, v65 dst_sel:DWORD dst_unused:UNUSED_PAD src0_sel:WORD_1 src1_sel:DWORD
	v_add3_u32 v69, v80, v69, s36
	v_add3_u32 v74, v78, v74, s36
	v_add3_u32 v68, v77, v68, s36
	v_add3_u32 v37, v79, v37, s36
	v_and_b32_e32 v69, 0xffff0000, v69
	v_and_b32_e32 v74, 0xffff0000, v74
	v_or_b32_sdwa v69, v69, v37 dst_sel:DWORD dst_unused:UNUSED_PAD src0_sel:DWORD src1_sel:WORD_1
	v_or_b32_sdwa v68, v74, v68 dst_sel:DWORD dst_unused:UNUSED_PAD src0_sel:DWORD src1_sel:WORD_1
	global_store_dwordx4 v[72:73], v[66:69], off
	ds_read_b32 v37, v49
	ds_read_b32 v74, v49 offset:516
	ds_read_b32 v75, v49 offset:1032
	ds_read_b32 v76, v49 offset:1548
	ds_read_b32 v77, v49 offset:2064
	ds_read_b32 v78, v49 offset:2580
	ds_read_b32 v79, v49 offset:3096
	ds_read_b32 v80, v49 offset:3612
	v_add_u32_e32 v66, s8, v48
	v_lshlrev_b32_e32 v67, 1, v66
	v_and_b32_e32 v67, 0xffffffe0, v67
	v_add3_u32 v67, s1, v50, v67
	v_cndmask_b32_e32 v66, v67, v66, vcc
	v_ashrrev_i32_e32 v69, 31, v66
	v_mad_u64_u32 v[66:67], s[2:3], v66, s29, 0
	v_mov_b32_e32 v68, v67
	v_mad_u64_u32 v[68:69], s[2:3], v69, s29, v[68:69]
	v_mov_b32_e32 v67, v68
	v_lshl_add_u64 v[72:73], v[66:67], 1, v[70:71]
	s_waitcnt lgkmcnt(7)
	v_and_b32_sdwa v67, v37, v65 dst_sel:DWORD dst_unused:UNUSED_PAD src0_sel:WORD_1 src1_sel:DWORD
	v_add3_u32 v37, v37, v67, s36
	s_waitcnt lgkmcnt(4)
	v_and_b32_sdwa v67, v76, v65 dst_sel:DWORD dst_unused:UNUSED_PAD src0_sel:WORD_1 src1_sel:DWORD
	v_and_b32_sdwa v68, v74, v65 dst_sel:DWORD dst_unused:UNUSED_PAD src0_sel:WORD_1 src1_sel:DWORD
	v_and_b32_sdwa v66, v75, v65 dst_sel:DWORD dst_unused:UNUSED_PAD src0_sel:WORD_1 src1_sel:DWORD
	v_add3_u32 v67, v76, v67, s36
	v_add3_u32 v68, v74, v68, s36
	v_add3_u32 v66, v75, v66, s36
	v_and_b32_e32 v67, 0xffff0000, v67
	v_and_b32_e32 v68, 0xffff0000, v68
	s_waitcnt lgkmcnt(0)
	v_and_b32_sdwa v69, v80, v65 dst_sel:DWORD dst_unused:UNUSED_PAD src0_sel:WORD_1 src1_sel:DWORD
	v_and_b32_sdwa v74, v78, v65 dst_sel:DWORD dst_unused:UNUSED_PAD src0_sel:WORD_1 src1_sel:DWORD
	v_or_b32_sdwa v67, v67, v66 dst_sel:DWORD dst_unused:UNUSED_PAD src0_sel:DWORD src1_sel:WORD_1
	v_or_b32_sdwa v66, v68, v37 dst_sel:DWORD dst_unused:UNUSED_PAD src0_sel:DWORD src1_sel:WORD_1
	v_and_b32_sdwa v37, v79, v65 dst_sel:DWORD dst_unused:UNUSED_PAD src0_sel:WORD_1 src1_sel:DWORD
	v_and_b32_sdwa v68, v77, v65 dst_sel:DWORD dst_unused:UNUSED_PAD src0_sel:WORD_1 src1_sel:DWORD
	v_add3_u32 v69, v80, v69, s36
	v_add3_u32 v74, v78, v74, s36
	v_add3_u32 v68, v77, v68, s36
	v_add3_u32 v37, v79, v37, s36
	v_and_b32_e32 v69, 0xffff0000, v69
	v_and_b32_e32 v74, 0xffff0000, v74
	v_or_b32_sdwa v69, v69, v37 dst_sel:DWORD dst_unused:UNUSED_PAD src0_sel:DWORD src1_sel:WORD_1
	v_or_b32_sdwa v68, v74, v68 dst_sel:DWORD dst_unused:UNUSED_PAD src0_sel:DWORD src1_sel:WORD_1
	global_store_dwordx4 v[72:73], v[66:69], off
	ds_read_b32 v37, v52
	ds_read_b32 v74, v52 offset:516
	ds_read_b32 v75, v52 offset:1032
	ds_read_b32 v76, v52 offset:1548
	ds_read_b32 v77, v52 offset:2064
	ds_read_b32 v78, v52 offset:2580
	ds_read_b32 v79, v52 offset:3096
	ds_read_b32 v80, v52 offset:3612
	v_add_u32_e32 v66, s8, v51
	v_lshlrev_b32_e32 v67, 1, v66
	v_and_b32_e32 v67, 0xffffffe0, v67
	v_add3_u32 v67, s1, v53, v67
	v_cndmask_b32_e32 v66, v67, v66, vcc
	v_ashrrev_i32_e32 v69, 31, v66
	v_mad_u64_u32 v[66:67], s[2:3], v66, s29, 0
	v_mov_b32_e32 v68, v67
	v_mad_u64_u32 v[68:69], s[2:3], v69, s29, v[68:69]
	v_mov_b32_e32 v67, v68
	v_lshl_add_u64 v[72:73], v[66:67], 1, v[70:71]
	s_waitcnt lgkmcnt(7)
	v_and_b32_sdwa v67, v37, v65 dst_sel:DWORD dst_unused:UNUSED_PAD src0_sel:WORD_1 src1_sel:DWORD
	v_add3_u32 v37, v37, v67, s36
	s_waitcnt lgkmcnt(4)
	v_and_b32_sdwa v67, v76, v65 dst_sel:DWORD dst_unused:UNUSED_PAD src0_sel:WORD_1 src1_sel:DWORD
	v_and_b32_sdwa v68, v74, v65 dst_sel:DWORD dst_unused:UNUSED_PAD src0_sel:WORD_1 src1_sel:DWORD
	v_and_b32_sdwa v66, v75, v65 dst_sel:DWORD dst_unused:UNUSED_PAD src0_sel:WORD_1 src1_sel:DWORD
	v_add3_u32 v67, v76, v67, s36
	v_add3_u32 v68, v74, v68, s36
	v_add3_u32 v66, v75, v66, s36
	v_and_b32_e32 v67, 0xffff0000, v67
	v_and_b32_e32 v68, 0xffff0000, v68
	s_waitcnt lgkmcnt(0)
	v_and_b32_sdwa v69, v80, v65 dst_sel:DWORD dst_unused:UNUSED_PAD src0_sel:WORD_1 src1_sel:DWORD
	v_and_b32_sdwa v74, v78, v65 dst_sel:DWORD dst_unused:UNUSED_PAD src0_sel:WORD_1 src1_sel:DWORD
	v_or_b32_sdwa v67, v67, v66 dst_sel:DWORD dst_unused:UNUSED_PAD src0_sel:DWORD src1_sel:WORD_1
	v_or_b32_sdwa v66, v68, v37 dst_sel:DWORD dst_unused:UNUSED_PAD src0_sel:DWORD src1_sel:WORD_1
	v_and_b32_sdwa v37, v79, v65 dst_sel:DWORD dst_unused:UNUSED_PAD src0_sel:WORD_1 src1_sel:DWORD
	v_and_b32_sdwa v68, v77, v65 dst_sel:DWORD dst_unused:UNUSED_PAD src0_sel:WORD_1 src1_sel:DWORD
	v_add3_u32 v69, v80, v69, s36
	v_add3_u32 v74, v78, v74, s36
	v_add3_u32 v68, v77, v68, s36
	v_add3_u32 v37, v79, v37, s36
	v_and_b32_e32 v69, 0xffff0000, v69
	v_and_b32_e32 v74, 0xffff0000, v74
	v_or_b32_sdwa v69, v69, v37 dst_sel:DWORD dst_unused:UNUSED_PAD src0_sel:DWORD src1_sel:WORD_1
	v_or_b32_sdwa v68, v74, v68 dst_sel:DWORD dst_unused:UNUSED_PAD src0_sel:DWORD src1_sel:WORD_1
	global_store_dwordx4 v[72:73], v[66:69], off
	ds_read_b32 v37, v55
	ds_read_b32 v72, v55 offset:516
	ds_read_b32 v73, v55 offset:1032
	ds_read_b32 v74, v55 offset:1548
	ds_read_b32 v75, v55 offset:2064
	ds_read_b32 v76, v55 offset:2580
	ds_read_b32 v77, v55 offset:3096
	ds_read_b32 v78, v55 offset:3612
	v_add_u32_e32 v66, s8, v54
	v_lshlrev_b32_e32 v67, 1, v66
	v_and_b32_e32 v67, 0xffffffe0, v67
	v_add3_u32 v67, s1, v56, v67
	v_cndmask_b32_e32 v66, v67, v66, vcc
	v_ashrrev_i32_e32 v69, 31, v66
	v_mad_u64_u32 v[66:67], s[2:3], v66, s29, 0
	v_mov_b32_e32 v68, v67
	v_mad_u64_u32 v[68:69], s[2:3], v69, s29, v[68:69]
	v_mov_b32_e32 v67, v68
	v_lshl_add_u64 v[70:71], v[66:67], 1, v[70:71]
	s_waitcnt lgkmcnt(7)
	v_and_b32_sdwa v67, v37, v65 dst_sel:DWORD dst_unused:UNUSED_PAD src0_sel:WORD_1 src1_sel:DWORD
	v_add3_u32 v37, v37, v67, s36
	s_waitcnt lgkmcnt(4)
	v_and_b32_sdwa v67, v74, v65 dst_sel:DWORD dst_unused:UNUSED_PAD src0_sel:WORD_1 src1_sel:DWORD
	v_and_b32_sdwa v68, v72, v65 dst_sel:DWORD dst_unused:UNUSED_PAD src0_sel:WORD_1 src1_sel:DWORD
	v_and_b32_sdwa v66, v73, v65 dst_sel:DWORD dst_unused:UNUSED_PAD src0_sel:WORD_1 src1_sel:DWORD
	v_add3_u32 v67, v74, v67, s36
	v_add3_u32 v68, v72, v68, s36
	v_add3_u32 v66, v73, v66, s36
	v_and_b32_e32 v67, 0xffff0000, v67
	v_and_b32_e32 v68, 0xffff0000, v68
	s_waitcnt lgkmcnt(0)
	v_and_b32_sdwa v69, v78, v65 dst_sel:DWORD dst_unused:UNUSED_PAD src0_sel:WORD_1 src1_sel:DWORD
	v_and_b32_sdwa v72, v76, v65 dst_sel:DWORD dst_unused:UNUSED_PAD src0_sel:WORD_1 src1_sel:DWORD
	v_or_b32_sdwa v67, v67, v66 dst_sel:DWORD dst_unused:UNUSED_PAD src0_sel:DWORD src1_sel:WORD_1
	v_or_b32_sdwa v66, v68, v37 dst_sel:DWORD dst_unused:UNUSED_PAD src0_sel:DWORD src1_sel:WORD_1
	v_and_b32_sdwa v37, v77, v65 dst_sel:DWORD dst_unused:UNUSED_PAD src0_sel:WORD_1 src1_sel:DWORD
	v_and_b32_sdwa v68, v75, v65 dst_sel:DWORD dst_unused:UNUSED_PAD src0_sel:WORD_1 src1_sel:DWORD
	v_add3_u32 v69, v78, v69, s36
	v_add3_u32 v72, v76, v72, s36
	v_add3_u32 v68, v75, v68, s36
	v_add3_u32 v37, v77, v37, s36
	v_and_b32_e32 v69, 0xffff0000, v69
	v_and_b32_e32 v72, 0xffff0000, v72
	v_or_b32_sdwa v69, v69, v37 dst_sel:DWORD dst_unused:UNUSED_PAD src0_sel:DWORD src1_sel:WORD_1
	v_or_b32_sdwa v68, v72, v68 dst_sel:DWORD dst_unused:UNUSED_PAD src0_sel:DWORD src1_sel:WORD_1
	s_add_i32 s34, s34, s38
	s_add_i32 s35, s35, s38
	s_andn2_b64 vcc, exec, s[18:19]
	s_mov_b32 s1, s37
	s_mov_b32 s17, s26
	s_mov_b32 s8, s22
	s_mov_b32 s16, s10
	s_mov_b32 s29, s27
	s_mov_b64 s[2:3], s[20:21]
	global_store_dwordx4 v[70:71], v[66:69], off
	s_barrier
	s_cbranch_vccz .LBB0_240

.LBB0_1942:
	s_waitcnt vmcnt(11)
	v_add_u32_e32 v2, 0x800, v34
	s_lshr_b32 s4, s8, 7
	v_ashrrev_i32_e32 v42, 5, v2
	v_cvt_f32_u32_e32 v2, s4
	s_sub_i32 s11, 0, s4
	s_abs_i32 s10, s9
	s_ashr_i32 s5, s9, 31
	v_rcp_iflag_f32_e32 v2, v2
	v_add_u32_e32 v3, 0xa00, v34
	v_ashrrev_i32_e32 v43, 5, v3
	v_add_u32_e32 v3, 0xc00, v34
	v_mul_f32_e32 v2, 0x4f7ffffe, v2
	v_cvt_u32_f32_e32 v2, v2
	v_lshlrev_b32_e32 v1, 2, v34
	v_ashrrev_i32_e32 v44, 5, v3
	v_add_u32_e32 v3, 0xe00, v34
	v_readfirstlane_b32 s12, v2
	s_mul_i32 s11, s11, s12
	s_mul_hi_u32 s11, s12, s11
	s_add_i32 s12, s12, s11
	s_mul_hi_u32 s11, s10, s12
	s_mul_i32 s12, s11, s4
	s_sub_i32 s10, s10, s12
	s_add_i32 s12, s11, 1
	s_sub_i32 s13, s10, s4
	s_cmp_ge_u32 s10, s4
	s_cselect_b32 s11, s12, s11
	s_cselect_b32 s10, s13, s10
	s_add_i32 s12, s11, 1
	s_cmp_ge_u32 s10, s4
	s_cselect_b32 s10, s12, s11
	s_xor_b32 s10, s10, s5
	s_sub_i32 s12, s10, s5
	s_mul_i32 s4, s12, s4
	s_sub_i32 s4, s9, s4
	s_lshl_b32 s4, s4, 7
	s_ashr_i32 s5, s4, 31
	s_lshl_b64 s[10:11], s[4:5], 2
	s_add_u32 s6, s6, s10
	v_and_b32_e32 v38, 0x7c, v1
	v_ashrrev_i32_e32 v45, 5, v3
	s_addc_u32 s7, s7, s11
	s_lshl_b32 s14, s12, 7
	v_mov_b32_e32 v37, 0
	v_lshlrev_b32_e32 v36, 2, v38
	v_add_u32_e32 v4, s14, v45
	v_lshl_add_u64 v[2:3], s[6:7], 0, v[36:37]
	s_waitcnt vmcnt(10)
	v_ashrrev_i32_e32 v7, 31, v4
	v_mad_u64_u32 v[4:5], s[6:7], v4, s8, 0
	v_mov_b32_e32 v6, v5
	v_mad_u64_u32 v[6:7], s[6:7], v7, s8, v[6:7]
	v_mov_b32_e32 v5, v6
	v_add_u32_e32 v6, s14, v44
	v_ashrrev_i32_e32 v9, 31, v6
	v_mad_u64_u32 v[6:7], s[6:7], v6, s8, 0
	v_mov_b32_e32 v8, v7
	v_mad_u64_u32 v[8:9], s[6:7], v9, s8, v[8:9]
	v_lshl_add_u64 v[4:5], v[4:5], 2, v[2:3]
	v_mov_b32_e32 v7, v8
	v_lshl_add_u64 v[6:7], v[6:7], 2, v[2:3]
	global_load_dwordx4 v[30:33], v[4:5], off
	global_load_dwordx4 v[26:29], v[6:7], off
	v_add_u32_e32 v4, s14, v43
	v_ashrrev_i32_e32 v7, 31, v4
	v_mad_u64_u32 v[4:5], s[6:7], v4, s8, 0
	v_mov_b32_e32 v6, v5
	v_mad_u64_u32 v[6:7], s[6:7], v7, s8, v[6:7]
	v_mov_b32_e32 v5, v6
	v_add_u32_e32 v6, s14, v42
	v_ashrrev_i32_e32 v9, 31, v6
	v_mad_u64_u32 v[6:7], s[6:7], v6, s8, 0
	v_mov_b32_e32 v8, v7
	v_add_u32_e32 v55, 0x600, v34
	v_mad_u64_u32 v[8:9], s[6:7], v9, s8, v[8:9]
	v_ashrrev_i32_e32 v41, 5, v55
	v_lshl_add_u64 v[4:5], v[4:5], 2, v[2:3]
	v_mov_b32_e32 v7, v8
	v_lshl_add_u64 v[6:7], v[6:7], 2, v[2:3]
	global_load_dwordx4 v[22:25], v[4:5], off
	global_load_dwordx4 v[18:21], v[6:7], off
	v_add_u32_e32 v4, s14, v41
	v_ashrrev_i32_e32 v7, 31, v4
	v_mad_u64_u32 v[4:5], s[6:7], v4, s8, 0
	v_add_u32_e32 v52, 0x400, v34
	v_mov_b32_e32 v6, v5
	v_ashrrev_i32_e32 v40, 5, v52
	v_mad_u64_u32 v[6:7], s[6:7], v7, s8, v[6:7]
	v_mov_b32_e32 v5, v6
	v_add_u32_e32 v6, s14, v40
	v_ashrrev_i32_e32 v9, 31, v6
	v_mad_u64_u32 v[6:7], s[6:7], v6, s8, 0
	v_mov_b32_e32 v8, v7
	v_add_u32_e32 v39, 0x200, v34
	v_mad_u64_u32 v[8:9], s[6:7], v9, s8, v[8:9]
	v_ashrrev_i32_e32 v35, 5, v39
	v_lshl_add_u64 v[4:5], v[4:5], 2, v[2:3]
	v_mov_b32_e32 v7, v8
	v_lshl_add_u64 v[6:7], v[6:7], 2, v[2:3]
	global_load_dwordx4 v[14:17], v[4:5], off
	global_load_dwordx4 v[10:13], v[6:7], off
	v_add_u32_e32 v4, s14, v35
	v_ashrrev_i32_e32 v7, 31, v4
	v_mad_u64_u32 v[4:5], s[6:7], v4, s8, 0
	v_mov_b32_e32 v6, v5
	v_ashrrev_i32_e32 v1, 5, v34
	v_mad_u64_u32 v[6:7], s[6:7], v7, s8, v[6:7]
	v_mov_b32_e32 v5, v6
	v_add_u32_e32 v6, s14, v1
	v_ashrrev_i32_e32 v9, 31, v6
	v_mad_u64_u32 v[6:7], s[6:7], v6, s8, 0
	v_mov_b32_e32 v8, v7
	v_mad_u64_u32 v[8:9], s[6:7], v9, s8, v[8:9]
	v_mov_b32_e32 v7, v8
	v_lshl_add_u64 v[4:5], v[4:5], 2, v[2:3]
	v_lshl_add_u64 v[2:3], v[6:7], 2, v[2:3]
	global_load_dwordx4 v[6:9], v[4:5], off
	s_nop 0
	global_load_dwordx4 v[2:5], v[2:3], off
	v_lshlrev_b32_e32 v46, 3, v34
	v_and_b32_e32 v66, 0x78, v46
	s_movk_i32 s5, 0x204
	v_readlane_b32 s12, v251, 60
	v_mad_u32_u24 v56, v66, s5, 0
	v_mul_lo_u32 v58, v1, s5
	v_mul_lo_u32 v59, v35, s5
	v_mul_lo_u32 v60, v40, s5
	v_mul_lo_u32 v61, v41, s5
	v_mul_lo_u32 v62, v42, s5
	v_mul_lo_u32 v63, v43, s5
	v_mul_lo_u32 v64, v44, s5
	v_mul_lo_u32 v65, v45, s5
	v_readlane_b32 s13, v251, 61
	s_add_u32 s5, s12, 0x1e940000
	s_addc_u32 s26, s13, 0
	s_add_u32 s8, s12, 0x16940000
	s_addc_u32 s9, s13, 0
	s_add_u32 s10, s12, 0x16140000
	s_addc_u32 s11, s13, 0
	s_add_u32 s27, s12, 0x15540000
	s_addc_u32 s28, s13, 0
	v_add_u32_e32 v36, 0, v36
	v_ashrrev_i32_e32 v46, 4, v34
	v_ashrrev_i32_e32 v49, 4, v39
	v_ashrrev_i32_e32 v52, 4, v52
	v_ashrrev_i32_e32 v55, 4, v55
	s_add_u32 s12, s12, 0x11f40000
	s_mov_b32 s7, 0
	v_lshl_add_u32 v47, v46, 2, v56
	v_and_b32_e32 v48, 15, v46
	v_lshl_add_u32 v50, v49, 2, v56
	v_and_b32_e32 v51, 15, v49
	v_lshl_add_u32 v53, v52, 2, v56
	v_and_b32_e32 v54, 15, v52
	v_lshl_add_u32 v56, v55, 2, v56
	v_and_b32_e32 v57, 15, v55
	s_addc_u32 s13, s13, 0
	s_add_i32 s29, s16, 0x15e1
	s_mov_b32 s30, 17
	v_add_u32_e32 v58, v36, v58
	v_add_u32_e32 v59, v36, v59
	v_add_u32_e32 v60, v36, v60
	v_add_u32_e32 v61, v36, v61
	v_add_u32_e32 v62, v36, v62
	v_add_u32_e32 v63, v36, v63
	v_add_u32_e32 v64, v36, v64
	v_add_u32_e32 v65, v36, v65
	v_lshlrev_b32_e32 v36, 2, v38
	v_lshlrev_b32_e32 v38, 1, v66
	s_movk_i32 s31, 0x7fff
	v_mov_b32_e32 v66, 1
	s_mov_b32 s24, s15
	s_mov_b32 s25, s0
	s_mov_b64 s[18:19], s[2:3]
	v_readlane_b32 s42, v251, 58
	v_readlane_b32 s43, v251, 59
	s_branch .LBB0_1946

.LBB0_1944:
	s_lshr_b32 s20, s36, 7
	v_cvt_f32_u32_e32 v2, s20
	s_sub_i32 s34, 0, s20
	s_abs_i32 s21, s37
	s_ashr_i32 s6, s37, 31
	v_rcp_iflag_f32_e32 v2, v2
	s_nop 0
	v_mul_f32_e32 v2, 0x4f7ffffe, v2
	v_cvt_u32_f32_e32 v2, v2
	s_nop 0
	v_readfirstlane_b32 s38, v2
	s_mul_i32 s34, s34, s38
	s_mul_hi_u32 s34, s38, s34
	s_add_i32 s38, s38, s34
	s_mul_hi_u32 s34, s21, s38
	s_mul_i32 s38, s34, s20
	s_sub_i32 s21, s21, s38
	s_add_i32 s39, s34, 1
	s_sub_i32 s38, s21, s20
	s_cmp_ge_u32 s21, s20
	s_cselect_b32 s34, s39, s34
	s_cselect_b32 s21, s38, s21
	s_add_i32 s38, s34, 1
	s_cmp_ge_u32 s21, s20
	s_cselect_b32 s21, s38, s34
	s_xor_b32 s21, s21, s6
	s_sub_i32 s21, s21, s6
	s_lshl_b32 s6, s21, 7
	s_mul_i32 s21, s21, s20
	s_sub_i32 s20, s37, s21
	s_lshl_b32 s20, s20, 7
	s_ashr_i32 s21, s20, 31
	s_lshl_b64 s[38:39], s[20:21], 2
	s_add_u32 s22, s22, s38
	v_add_u32_e32 v2, s6, v1
	s_addc_u32 s23, s23, s39
	v_add_u32_e32 v10, s6, v40
	v_add_u32_e32 v18, s6, v42
	v_add_u32_e32 v28, s6, v44
	v_ashrrev_i32_e32 v5, 31, v2
	v_lshl_add_u64 v[26:27], s[22:23], 0, v[36:37]
	v_mad_u64_u32 v[2:3], s[22:23], v2, s36, 0
	v_ashrrev_i32_e32 v13, 31, v10
	v_mad_u64_u32 v[10:11], s[22:23], v10, s36, 0
	v_ashrrev_i32_e32 v21, 31, v18
	v_mad_u64_u32 v[18:19], s[22:23], v18, s36, 0
	v_ashrrev_i32_e32 v31, 31, v28
	v_mad_u64_u32 v[28:29], s[22:23], v28, s36, 0
	v_mov_b32_e32 v4, v3
	v_mov_b32_e32 v12, v11
	v_mov_b32_e32 v20, v19
	v_mov_b32_e32 v30, v29
	v_mad_u64_u32 v[4:5], s[22:23], v5, s36, v[4:5]
	v_mad_u64_u32 v[12:13], s[22:23], v13, s36, v[12:13]
	v_mad_u64_u32 v[20:21], s[22:23], v21, s36, v[20:21]
	v_mad_u64_u32 v[30:31], s[22:23], v31, s36, v[30:31]
	v_mov_b32_e32 v3, v4
	v_add_u32_e32 v4, s6, v35
	v_mov_b32_e32 v11, v12
	v_add_u32_e32 v12, s6, v41
	v_mov_b32_e32 v19, v20
	v_add_u32_e32 v20, s6, v43
	v_mov_b32_e32 v29, v30
	v_add_u32_e32 v30, s6, v45
	v_ashrrev_i32_e32 v7, 31, v4
	v_mad_u64_u32 v[4:5], s[22:23], v4, s36, 0
	v_ashrrev_i32_e32 v15, 31, v12
	v_mad_u64_u32 v[12:13], s[22:23], v12, s36, 0
	v_ashrrev_i32_e32 v23, 31, v20
	v_mad_u64_u32 v[20:21], s[22:23], v20, s36, 0
	v_ashrrev_i32_e32 v33, 31, v30
	v_mad_u64_u32 v[30:31], s[22:23], v30, s36, 0
	v_mov_b32_e32 v6, v5
	v_mov_b32_e32 v14, v13
	v_mov_b32_e32 v22, v21
	v_mov_b32_e32 v32, v31
	v_mad_u64_u32 v[6:7], s[22:23], v7, s36, v[6:7]
	v_mad_u64_u32 v[14:15], s[22:23], v15, s36, v[14:15]
	v_mad_u64_u32 v[22:23], s[22:23], v23, s36, v[22:23]
	v_mad_u64_u32 v[32:33], s[22:23], v33, s36, v[32:33]
	v_mov_b32_e32 v5, v6
	v_mov_b32_e32 v13, v14
	v_mov_b32_e32 v21, v22
	v_mov_b32_e32 v31, v32
	v_lshl_add_u64 v[2:3], v[2:3], 2, v[26:27]
	v_lshl_add_u64 v[6:7], v[4:5], 2, v[26:27]
	v_lshl_add_u64 v[10:11], v[10:11], 2, v[26:27]
	v_lshl_add_u64 v[14:15], v[12:13], 2, v[26:27]
	v_lshl_add_u64 v[18:19], v[18:19], 2, v[26:27]
	v_lshl_add_u64 v[22:23], v[20:21], 2, v[26:27]
	v_lshl_add_u64 v[28:29], v[28:29], 2, v[26:27]
	v_lshl_add_u64 v[30:31], v[30:31], 2, v[26:27]
	global_load_dwordx4 v[2:5], v[2:3], off
	s_nop 0
	global_load_dwordx4 v[6:9], v[6:7], off
	s_nop 0
	global_load_dwordx4 v[10:13], v[10:11], off
	s_nop 0
	global_load_dwordx4 v[14:17], v[14:15], off
	s_nop 0
	global_load_dwordx4 v[18:21], v[18:19], off
	s_nop 0
	global_load_dwordx4 v[22:25], v[22:23], off
	s_nop 0
	global_load_dwordx4 v[26:29], v[28:29], off
	s_nop 0
	global_load_dwordx4 v[30:33], v[30:31], off
.LBB0_1945:
	s_add_i32 s30, s30, -1
	s_cmp_eq_u32 s15, 0
	v_add_u32_e32 v67, s4, v46
	v_lshlrev_b32_e32 v39, 1, v67
	s_cselect_b64 vcc, -1, 0
	s_ashr_i32 s15, s14, 31
	v_and_b32_e32 v39, 0xffffffe0, v39
	s_lshl_b64 s[14:15], s[14:15], 1
	v_add3_u32 v68, s1, v48, v39
	s_add_u32 s2, s2, s14
	s_addc_u32 s3, s3, s15
	v_mov_b32_e32 v39, v37
	v_cndmask_b32_e32 v67, v68, v67, vcc
	v_lshl_add_u64 v[72:73], s[2:3], 0, v[38:39]
	v_mad_u64_u32 v[68:69], s[2:3], v67, s0, 0
	v_ashrrev_i32_e32 v71, 31, v67
	v_mov_b32_e32 v70, v69
	v_mad_u64_u32 v[70:71], s[2:3], v71, s0, v[70:71]
	ds_read_b32 v39, v47
	ds_read_b32 v76, v47 offset:516
	ds_read_b32 v77, v47 offset:1032
	ds_read_b32 v78, v47 offset:1548
	ds_read_b32 v79, v47 offset:2064
	ds_read_b32 v80, v47 offset:2580
	ds_read_b32 v81, v47 offset:3096
	ds_read_b32 v82, v47 offset:3612
	v_mov_b32_e32 v69, v70
	v_lshl_add_u64 v[74:75], v[68:69], 1, v[72:73]
	s_waitcnt lgkmcnt(7)
	v_and_b32_sdwa v68, v39, v66 dst_sel:DWORD dst_unused:UNUSED_PAD src0_sel:WORD_1 src1_sel:DWORD
	v_add3_u32 v39, v39, v68, s31
	s_waitcnt lgkmcnt(4)
	v_and_b32_sdwa v68, v78, v66 dst_sel:DWORD dst_unused:UNUSED_PAD src0_sel:WORD_1 src1_sel:DWORD
	v_and_b32_sdwa v69, v76, v66 dst_sel:DWORD dst_unused:UNUSED_PAD src0_sel:WORD_1 src1_sel:DWORD
	v_and_b32_sdwa v67, v77, v66 dst_sel:DWORD dst_unused:UNUSED_PAD src0_sel:WORD_1 src1_sel:DWORD
	v_add3_u32 v68, v78, v68, s31
	v_add3_u32 v69, v76, v69, s31
	v_add3_u32 v67, v77, v67, s31
	v_and_b32_e32 v68, 0xffff0000, v68
	v_and_b32_e32 v70, 0xffff0000, v69
	v_or_b32_sdwa v69, v68, v67 dst_sel:DWORD dst_unused:UNUSED_PAD src0_sel:DWORD src1_sel:WORD_1
	v_or_b32_sdwa v68, v70, v39 dst_sel:DWORD dst_unused:UNUSED_PAD src0_sel:DWORD src1_sel:WORD_1
	s_waitcnt lgkmcnt(0)
	v_and_b32_sdwa v70, v82, v66 dst_sel:DWORD dst_unused:UNUSED_PAD src0_sel:WORD_1 src1_sel:DWORD
	v_and_b32_sdwa v71, v80, v66 dst_sel:DWORD dst_unused:UNUSED_PAD src0_sel:WORD_1 src1_sel:DWORD
	v_and_b32_sdwa v39, v81, v66 dst_sel:DWORD dst_unused:UNUSED_PAD src0_sel:WORD_1 src1_sel:DWORD
	v_and_b32_sdwa v67, v79, v66 dst_sel:DWORD dst_unused:UNUSED_PAD src0_sel:WORD_1 src1_sel:DWORD
	v_add3_u32 v70, v82, v70, s31
	v_add3_u32 v71, v80, v71, s31
	v_add3_u32 v67, v79, v67, s31
	v_add3_u32 v39, v81, v39, s31
	v_and_b32_e32 v70, 0xffff0000, v70
	v_and_b32_e32 v76, 0xffff0000, v71
	v_or_b32_sdwa v71, v70, v39 dst_sel:DWORD dst_unused:UNUSED_PAD src0_sel:DWORD src1_sel:WORD_1
	v_or_b32_sdwa v70, v76, v67 dst_sel:DWORD dst_unused:UNUSED_PAD src0_sel:DWORD src1_sel:WORD_1
	global_store_dwordx4 v[74:75], v[68:71], off
	ds_read_b32 v39, v50
	ds_read_b32 v67, v50 offset:516
	ds_read_b32 v76, v50 offset:1032
	ds_read_b32 v77, v50 offset:1548
	ds_read_b32 v78, v50 offset:2064
	ds_read_b32 v79, v50 offset:2580
	ds_read_b32 v80, v50 offset:3096
	ds_read_b32 v81, v50 offset:3612
	v_add_u32_e32 v68, s4, v49
	v_lshlrev_b32_e32 v69, 1, v68
	v_and_b32_e32 v69, 0xffffffe0, v69
	v_add3_u32 v69, s1, v51, v69
	v_cndmask_b32_e32 v68, v69, v68, vcc
	v_ashrrev_i32_e32 v71, 31, v68
	v_mad_u64_u32 v[68:69], s[2:3], v68, s0, 0
	v_mov_b32_e32 v70, v69
	v_mad_u64_u32 v[70:71], s[2:3], v71, s0, v[70:71]
	v_mov_b32_e32 v69, v70
	v_lshl_add_u64 v[74:75], v[68:69], 1, v[72:73]
	s_waitcnt lgkmcnt(7)
	v_and_b32_sdwa v69, v39, v66 dst_sel:DWORD dst_unused:UNUSED_PAD src0_sel:WORD_1 src1_sel:DWORD
	v_add3_u32 v39, v39, v69, s31
	s_waitcnt lgkmcnt(4)
	v_and_b32_sdwa v69, v77, v66 dst_sel:DWORD dst_unused:UNUSED_PAD src0_sel:WORD_1 src1_sel:DWORD
	v_and_b32_sdwa v70, v67, v66 dst_sel:DWORD dst_unused:UNUSED_PAD src0_sel:WORD_1 src1_sel:DWORD
	v_and_b32_sdwa v68, v76, v66 dst_sel:DWORD dst_unused:UNUSED_PAD src0_sel:WORD_1 src1_sel:DWORD
	v_add3_u32 v69, v77, v69, s31
	v_add3_u32 v67, v67, v70, s31
	v_add3_u32 v68, v76, v68, s31
	v_and_b32_e32 v69, 0xffff0000, v69
	v_and_b32_e32 v67, 0xffff0000, v67
	s_waitcnt lgkmcnt(0)
	v_and_b32_sdwa v70, v81, v66 dst_sel:DWORD dst_unused:UNUSED_PAD src0_sel:WORD_1 src1_sel:DWORD
	v_and_b32_sdwa v71, v79, v66 dst_sel:DWORD dst_unused:UNUSED_PAD src0_sel:WORD_1 src1_sel:DWORD
	v_or_b32_sdwa v69, v69, v68 dst_sel:DWORD dst_unused:UNUSED_PAD src0_sel:DWORD src1_sel:WORD_1
	v_or_b32_sdwa v68, v67, v39 dst_sel:DWORD dst_unused:UNUSED_PAD src0_sel:DWORD src1_sel:WORD_1
	v_and_b32_sdwa v39, v80, v66 dst_sel:DWORD dst_unused:UNUSED_PAD src0_sel:WORD_1 src1_sel:DWORD
	v_and_b32_sdwa v67, v78, v66 dst_sel:DWORD dst_unused:UNUSED_PAD src0_sel:WORD_1 src1_sel:DWORD
	v_add3_u32 v70, v81, v70, s31
	v_add3_u32 v71, v79, v71, s31
	v_add3_u32 v67, v78, v67, s31
	v_add3_u32 v39, v80, v39, s31
	v_and_b32_e32 v70, 0xffff0000, v70
	v_and_b32_e32 v76, 0xffff0000, v71
	v_or_b32_sdwa v71, v70, v39 dst_sel:DWORD dst_unused:UNUSED_PAD src0_sel:DWORD src1_sel:WORD_1
	v_or_b32_sdwa v70, v76, v67 dst_sel:DWORD dst_unused:UNUSED_PAD src0_sel:DWORD src1_sel:WORD_1
	global_store_dwordx4 v[74:75], v[68:71], off
	ds_read_b32 v39, v53
	ds_read_b32 v67, v53 offset:516
	ds_read_b32 v76, v53 offset:1032
	ds_read_b32 v77, v53 offset:1548
	ds_read_b32 v78, v53 offset:2064
	ds_read_b32 v79, v53 offset:2580
	ds_read_b32 v80, v53 offset:3096
	ds_read_b32 v81, v53 offset:3612
	v_add_u32_e32 v68, s4, v52
	v_lshlrev_b32_e32 v69, 1, v68
	v_and_b32_e32 v69, 0xffffffe0, v69
	v_add3_u32 v69, s1, v54, v69
	v_cndmask_b32_e32 v68, v69, v68, vcc
	v_ashrrev_i32_e32 v71, 31, v68
	v_mad_u64_u32 v[68:69], s[2:3], v68, s0, 0
	v_mov_b32_e32 v70, v69
	v_mad_u64_u32 v[70:71], s[2:3], v71, s0, v[70:71]
	v_mov_b32_e32 v69, v70
	v_lshl_add_u64 v[74:75], v[68:69], 1, v[72:73]
	s_waitcnt lgkmcnt(7)
	v_and_b32_sdwa v69, v39, v66 dst_sel:DWORD dst_unused:UNUSED_PAD src0_sel:WORD_1 src1_sel:DWORD
	v_add3_u32 v39, v39, v69, s31
	s_waitcnt lgkmcnt(4)
	v_and_b32_sdwa v69, v77, v66 dst_sel:DWORD dst_unused:UNUSED_PAD src0_sel:WORD_1 src1_sel:DWORD
	v_and_b32_sdwa v70, v67, v66 dst_sel:DWORD dst_unused:UNUSED_PAD src0_sel:WORD_1 src1_sel:DWORD
	v_and_b32_sdwa v68, v76, v66 dst_sel:DWORD dst_unused:UNUSED_PAD src0_sel:WORD_1 src1_sel:DWORD
	v_add3_u32 v69, v77, v69, s31
	v_add3_u32 v67, v67, v70, s31
	v_add3_u32 v68, v76, v68, s31
	v_and_b32_e32 v69, 0xffff0000, v69
	v_and_b32_e32 v67, 0xffff0000, v67
	s_waitcnt lgkmcnt(0)
	v_and_b32_sdwa v70, v81, v66 dst_sel:DWORD dst_unused:UNUSED_PAD src0_sel:WORD_1 src1_sel:DWORD
	v_and_b32_sdwa v71, v79, v66 dst_sel:DWORD dst_unused:UNUSED_PAD src0_sel:WORD_1 src1_sel:DWORD
	v_or_b32_sdwa v69, v69, v68 dst_sel:DWORD dst_unused:UNUSED_PAD src0_sel:DWORD src1_sel:WORD_1
	v_or_b32_sdwa v68, v67, v39 dst_sel:DWORD dst_unused:UNUSED_PAD src0_sel:DWORD src1_sel:WORD_1
	v_and_b32_sdwa v39, v80, v66 dst_sel:DWORD dst_unused:UNUSED_PAD src0_sel:WORD_1 src1_sel:DWORD
	v_and_b32_sdwa v67, v78, v66 dst_sel:DWORD dst_unused:UNUSED_PAD src0_sel:WORD_1 src1_sel:DWORD
	v_add3_u32 v70, v81, v70, s31
	v_add3_u32 v71, v79, v71, s31
	v_add3_u32 v67, v78, v67, s31
	v_add3_u32 v39, v80, v39, s31
	v_and_b32_e32 v70, 0xffff0000, v70
	v_and_b32_e32 v76, 0xffff0000, v71
	v_or_b32_sdwa v71, v70, v39 dst_sel:DWORD dst_unused:UNUSED_PAD src0_sel:DWORD src1_sel:WORD_1
	v_or_b32_sdwa v70, v76, v67 dst_sel:DWORD dst_unused:UNUSED_PAD src0_sel:DWORD src1_sel:WORD_1
	global_store_dwordx4 v[74:75], v[68:71], off
	ds_read_b32 v39, v56
	ds_read_b32 v67, v56 offset:516
	ds_read_b32 v74, v56 offset:1032
	ds_read_b32 v75, v56 offset:1548
	ds_read_b32 v76, v56 offset:2064
	ds_read_b32 v77, v56 offset:2580
	ds_read_b32 v78, v56 offset:3096
	ds_read_b32 v79, v56 offset:3612
	v_add_u32_e32 v68, s4, v55
	v_lshlrev_b32_e32 v69, 1, v68
	v_and_b32_e32 v69, 0xffffffe0, v69
	v_add3_u32 v69, s1, v57, v69
	v_cndmask_b32_e32 v68, v69, v68, vcc
	v_ashrrev_i32_e32 v71, 31, v68
	v_mad_u64_u32 v[68:69], s[2:3], v68, s0, 0
	v_mov_b32_e32 v70, v69
	v_mad_u64_u32 v[70:71], s[0:1], v71, s0, v[70:71]
	v_mov_b32_e32 v69, v70
	v_lshl_add_u64 v[72:73], v[68:69], 1, v[72:73]
	s_waitcnt lgkmcnt(7)
	v_and_b32_sdwa v69, v39, v66 dst_sel:DWORD dst_unused:UNUSED_PAD src0_sel:WORD_1 src1_sel:DWORD
	v_add3_u32 v39, v39, v69, s31
	s_waitcnt lgkmcnt(4)
	v_and_b32_sdwa v69, v75, v66 dst_sel:DWORD dst_unused:UNUSED_PAD src0_sel:WORD_1 src1_sel:DWORD
	v_and_b32_sdwa v70, v67, v66 dst_sel:DWORD dst_unused:UNUSED_PAD src0_sel:WORD_1 src1_sel:DWORD
	v_and_b32_sdwa v68, v74, v66 dst_sel:DWORD dst_unused:UNUSED_PAD src0_sel:WORD_1 src1_sel:DWORD
	v_add3_u32 v69, v75, v69, s31
	v_add3_u32 v67, v67, v70, s31
	v_add3_u32 v68, v74, v68, s31
	v_and_b32_e32 v69, 0xffff0000, v69
	v_and_b32_e32 v67, 0xffff0000, v67
	s_waitcnt lgkmcnt(0)
	v_and_b32_sdwa v70, v79, v66 dst_sel:DWORD dst_unused:UNUSED_PAD src0_sel:WORD_1 src1_sel:DWORD
	v_and_b32_sdwa v71, v77, v66 dst_sel:DWORD dst_unused:UNUSED_PAD src0_sel:WORD_1 src1_sel:DWORD
	v_or_b32_sdwa v69, v69, v68 dst_sel:DWORD dst_unused:UNUSED_PAD src0_sel:DWORD src1_sel:WORD_1
	v_or_b32_sdwa v68, v67, v39 dst_sel:DWORD dst_unused:UNUSED_PAD src0_sel:DWORD src1_sel:WORD_1
	v_and_b32_sdwa v39, v78, v66 dst_sel:DWORD dst_unused:UNUSED_PAD src0_sel:WORD_1 src1_sel:DWORD
	v_and_b32_sdwa v67, v76, v66 dst_sel:DWORD dst_unused:UNUSED_PAD src0_sel:WORD_1 src1_sel:DWORD
	v_add3_u32 v70, v79, v70, s31
	v_add3_u32 v71, v77, v71, s31
	v_add3_u32 v67, v76, v67, s31
	v_add3_u32 v39, v78, v39, s31
	v_and_b32_e32 v70, 0xffff0000, v70
	v_and_b32_e32 v74, 0xffff0000, v71
	v_or_b32_sdwa v71, v70, v39 dst_sel:DWORD dst_unused:UNUSED_PAD src0_sel:DWORD src1_sel:WORD_1
	v_or_b32_sdwa v70, v74, v67 dst_sel:DWORD dst_unused:UNUSED_PAD src0_sel:DWORD src1_sel:WORD_1
	s_add_i32 s29, s29, 1
	s_and_b64 vcc, exec, s[16:17]
	s_mov_b32 s34, s33
	s_mov_b32 s1, s35
	s_mov_b32 s15, s24
	s_mov_b32 s4, s20
	s_mov_b32 s14, s6
	s_mov_b32 s0, s25
	s_mov_b64 s[2:3], s[18:19]
	global_store_dwordx4 v[72:73], v[68:71], off
	s_barrier
	s_cbranch_vccnz .LBB0_1964

.LBB0_1991:
	s_waitcnt vmcnt(11)
	v_add_u32_e32 v2, 0x800, v34
	s_lshr_b32 s0, s8, 7
	v_ashrrev_i32_e32 v42, 5, v2
	v_cvt_f32_u32_e32 v2, s0
	s_sub_i32 s9, 0, s0
	s_abs_i32 s5, s10
	s_ashr_i32 s4, s10, 31
	v_rcp_iflag_f32_e32 v2, v2
	v_add_u32_e32 v3, 0xa00, v34
	v_ashrrev_i32_e32 v43, 5, v3
	v_add_u32_e32 v3, 0xc00, v34
	v_mul_f32_e32 v2, 0x4f7ffffe, v2
	v_cvt_u32_f32_e32 v2, v2
	v_lshlrev_b32_e32 v1, 2, v34
	v_ashrrev_i32_e32 v44, 5, v3
	v_add_u32_e32 v3, 0xe00, v34
	v_readfirstlane_b32 s11, v2
	s_mul_i32 s9, s9, s11
	s_mul_hi_u32 s9, s11, s9
	s_add_i32 s11, s11, s9
	s_mul_hi_u32 s9, s5, s11
	s_mul_i32 s11, s9, s0
	s_sub_i32 s5, s5, s11
	s_add_i32 s11, s9, 1
	s_sub_i32 s12, s5, s0
	s_cmp_ge_u32 s5, s0
	s_cselect_b32 s9, s11, s9
	s_cselect_b32 s5, s12, s5
	s_add_i32 s11, s9, 1
	s_cmp_ge_u32 s5, s0
	s_cselect_b32 s5, s11, s9
	s_xor_b32 s5, s5, s4
	s_sub_i32 s9, s5, s4
	s_mul_i32 s0, s9, s0
	s_sub_i32 s0, s10, s0
	s_lshl_b32 s4, s0, 7
	s_ashr_i32 s5, s4, 31
	s_lshl_b64 s[10:11], s[4:5], 2
	s_add_u32 s6, s6, s10
	v_and_b32_e32 v38, 0x7c, v1
	v_ashrrev_i32_e32 v45, 5, v3
	s_addc_u32 s7, s7, s11
	s_lshl_b32 s14, s9, 7
	v_mov_b32_e32 v37, 0
	v_lshlrev_b32_e32 v36, 2, v38
	v_add_u32_e32 v4, s14, v45
	v_lshl_add_u64 v[2:3], s[6:7], 0, v[36:37]
	s_waitcnt vmcnt(10)
	v_ashrrev_i32_e32 v7, 31, v4
	v_mad_u64_u32 v[4:5], s[6:7], v4, s8, 0
	v_mov_b32_e32 v6, v5
	v_mad_u64_u32 v[6:7], s[6:7], v7, s8, v[6:7]
	v_mov_b32_e32 v5, v6
	v_add_u32_e32 v6, s14, v44
	v_ashrrev_i32_e32 v9, 31, v6
	v_mad_u64_u32 v[6:7], s[6:7], v6, s8, 0
	v_mov_b32_e32 v8, v7
	v_mad_u64_u32 v[8:9], s[6:7], v9, s8, v[8:9]
	v_lshl_add_u64 v[4:5], v[4:5], 2, v[2:3]
	v_mov_b32_e32 v7, v8
	v_lshl_add_u64 v[6:7], v[6:7], 2, v[2:3]
	global_load_dwordx4 v[30:33], v[4:5], off
	global_load_dwordx4 v[26:29], v[6:7], off
	v_add_u32_e32 v4, s14, v43
	v_ashrrev_i32_e32 v7, 31, v4
	v_mad_u64_u32 v[4:5], s[6:7], v4, s8, 0
	v_mov_b32_e32 v6, v5
	v_mad_u64_u32 v[6:7], s[6:7], v7, s8, v[6:7]
	v_mov_b32_e32 v5, v6
	v_add_u32_e32 v6, s14, v42
	v_ashrrev_i32_e32 v9, 31, v6
	v_mad_u64_u32 v[6:7], s[6:7], v6, s8, 0
	v_mov_b32_e32 v8, v7
	v_add_u32_e32 v55, 0x600, v34
	v_mad_u64_u32 v[8:9], s[6:7], v9, s8, v[8:9]
	v_ashrrev_i32_e32 v41, 5, v55
	v_lshl_add_u64 v[4:5], v[4:5], 2, v[2:3]
	v_mov_b32_e32 v7, v8
	v_lshl_add_u64 v[6:7], v[6:7], 2, v[2:3]
	global_load_dwordx4 v[22:25], v[4:5], off
	global_load_dwordx4 v[18:21], v[6:7], off
	v_add_u32_e32 v4, s14, v41
	v_ashrrev_i32_e32 v7, 31, v4
	v_mad_u64_u32 v[4:5], s[6:7], v4, s8, 0
	v_add_u32_e32 v52, 0x400, v34
	v_mov_b32_e32 v6, v5
	v_ashrrev_i32_e32 v40, 5, v52
	v_mad_u64_u32 v[6:7], s[6:7], v7, s8, v[6:7]
	v_mov_b32_e32 v5, v6
	v_add_u32_e32 v6, s14, v40
	v_ashrrev_i32_e32 v9, 31, v6
	v_mad_u64_u32 v[6:7], s[6:7], v6, s8, 0
	v_mov_b32_e32 v8, v7
	v_add_u32_e32 v35, 0x200, v34
	v_mad_u64_u32 v[8:9], s[6:7], v9, s8, v[8:9]
	v_ashrrev_i32_e32 v39, 5, v35
	v_lshl_add_u64 v[4:5], v[4:5], 2, v[2:3]
	v_mov_b32_e32 v7, v8
	v_lshl_add_u64 v[6:7], v[6:7], 2, v[2:3]
	global_load_dwordx4 v[14:17], v[4:5], off
	global_load_dwordx4 v[10:13], v[6:7], off
	v_add_u32_e32 v4, s14, v39
	v_ashrrev_i32_e32 v7, 31, v4
	v_mad_u64_u32 v[4:5], s[6:7], v4, s8, 0
	v_mov_b32_e32 v6, v5
	v_ashrrev_i32_e32 v1, 5, v34
	v_mad_u64_u32 v[6:7], s[6:7], v7, s8, v[6:7]
	v_mov_b32_e32 v5, v6
	v_add_u32_e32 v6, s14, v1
	v_ashrrev_i32_e32 v9, 31, v6
	v_mad_u64_u32 v[6:7], s[6:7], v6, s8, 0
	v_mov_b32_e32 v8, v7
	v_mad_u64_u32 v[8:9], s[6:7], v9, s8, v[8:9]
	v_mov_b32_e32 v7, v8
	v_lshl_add_u64 v[4:5], v[4:5], 2, v[2:3]
	v_lshl_add_u64 v[2:3], v[6:7], 2, v[2:3]
	global_load_dwordx4 v[6:9], v[4:5], off
	s_nop 0
	global_load_dwordx4 v[2:5], v[2:3], off
	v_lshlrev_b32_e32 v46, 3, v34
	v_and_b32_e32 v66, 0x78, v46
	s_movk_i32 s0, 0x204
	v_readlane_b32 s12, v251, 60
	v_mad_u32_u24 v56, v66, s0, 0
	v_mul_lo_u32 v58, v1, s0
	v_mul_lo_u32 v59, v39, s0
	v_mul_lo_u32 v60, v40, s0
	v_mul_lo_u32 v61, v41, s0
	v_mul_lo_u32 v62, v42, s0
	v_mul_lo_u32 v63, v43, s0
	v_mul_lo_u32 v64, v44, s0
	v_mul_lo_u32 v65, v45, s0
	v_readlane_b32 s13, v251, 61
	s_add_u32 s0, s12, 0x1e940000
	s_addc_u32 s5, s13, 0
	s_add_u32 s8, s12, 0x16940000
	s_addc_u32 s9, s13, 0
	s_add_u32 s10, s12, 0x16140000
	s_addc_u32 s11, s13, 0
	s_add_u32 s27, s12, 0x15540000
	s_addc_u32 s28, s13, 0
	v_add_u32_e32 v36, 0, v36
	v_ashrrev_i32_e32 v46, 4, v34
	v_ashrrev_i32_e32 v49, 4, v35
	v_ashrrev_i32_e32 v52, 4, v52
	v_ashrrev_i32_e32 v55, 4, v55
	s_add_u32 s12, s12, 0x11f40000
	s_mov_b32 s7, 0
	v_lshl_add_u32 v47, v46, 2, v56
	v_and_b32_e32 v48, 15, v46
	v_lshl_add_u32 v50, v49, 2, v56
	v_and_b32_e32 v51, 15, v49
	v_lshl_add_u32 v53, v52, 2, v56
	v_and_b32_e32 v54, 15, v52
	v_lshl_add_u32 v56, v55, 2, v56
	v_and_b32_e32 v57, 15, v55
	s_addc_u32 s13, s13, 0
	s_add_i32 s29, s16, 0xfffffce1
	s_mov_b32 s30, 25
	v_add_u32_e32 v58, v36, v58
	v_add_u32_e32 v59, v36, v59
	v_add_u32_e32 v60, v36, v60
	v_add_u32_e32 v61, v36, v61
	v_add_u32_e32 v62, v36, v62
	v_add_u32_e32 v63, v36, v63
	v_add_u32_e32 v64, v36, v64
	v_add_u32_e32 v65, v36, v65
	v_lshlrev_b32_e32 v36, 2, v38
	v_lshlrev_b32_e32 v34, 1, v66
	s_movk_i32 s31, 0x7fff
	v_mov_b32_e32 v38, 1
	s_mov_b32 s24, s15
	s_mov_b32 s25, s26
	s_mov_b64 s[18:19], s[2:3]
	s_branch .LBB0_1995

.LBB0_1993:
	s_lshr_b32 s20, s36, 7
	v_cvt_f32_u32_e32 v2, s20
	s_sub_i32 s34, 0, s20
	s_abs_i32 s21, s37
	s_ashr_i32 s6, s37, 31
	v_rcp_iflag_f32_e32 v2, v2
	s_nop 0
	v_mul_f32_e32 v2, 0x4f7ffffe, v2
	v_cvt_u32_f32_e32 v2, v2
	s_nop 0
	v_readfirstlane_b32 s38, v2
	s_mul_i32 s34, s34, s38
	s_mul_hi_u32 s34, s38, s34
	s_add_i32 s38, s38, s34
	s_mul_hi_u32 s34, s21, s38
	s_mul_i32 s38, s34, s20
	s_sub_i32 s21, s21, s38
	s_add_i32 s39, s34, 1
	s_sub_i32 s38, s21, s20
	s_cmp_ge_u32 s21, s20
	s_cselect_b32 s34, s39, s34
	s_cselect_b32 s21, s38, s21
	s_add_i32 s38, s34, 1
	s_cmp_ge_u32 s21, s20
	s_cselect_b32 s21, s38, s34
	s_xor_b32 s21, s21, s6
	s_sub_i32 s21, s21, s6
	s_lshl_b32 s6, s21, 7
	s_mul_i32 s21, s21, s20
	s_sub_i32 s20, s37, s21
	s_lshl_b32 s20, s20, 7
	s_ashr_i32 s21, s20, 31
	s_lshl_b64 s[38:39], s[20:21], 2
	s_add_u32 s22, s22, s38
	v_add_u32_e32 v2, s6, v1
	s_addc_u32 s23, s23, s39
	v_add_u32_e32 v10, s6, v40
	v_add_u32_e32 v18, s6, v42
	v_add_u32_e32 v28, s6, v44
	v_ashrrev_i32_e32 v5, 31, v2
	v_lshl_add_u64 v[26:27], s[22:23], 0, v[36:37]
	v_mad_u64_u32 v[2:3], s[22:23], v2, s36, 0
	v_ashrrev_i32_e32 v13, 31, v10
	v_mad_u64_u32 v[10:11], s[22:23], v10, s36, 0
	v_ashrrev_i32_e32 v21, 31, v18
	v_mad_u64_u32 v[18:19], s[22:23], v18, s36, 0
	v_ashrrev_i32_e32 v31, 31, v28
	v_mad_u64_u32 v[28:29], s[22:23], v28, s36, 0
	v_mov_b32_e32 v4, v3
	v_mov_b32_e32 v12, v11
	v_mov_b32_e32 v20, v19
	v_mov_b32_e32 v30, v29
	v_mad_u64_u32 v[4:5], s[22:23], v5, s36, v[4:5]
	v_mad_u64_u32 v[12:13], s[22:23], v13, s36, v[12:13]
	v_mad_u64_u32 v[20:21], s[22:23], v21, s36, v[20:21]
	v_mad_u64_u32 v[30:31], s[22:23], v31, s36, v[30:31]
	v_mov_b32_e32 v3, v4
	v_add_u32_e32 v4, s6, v39
	v_mov_b32_e32 v11, v12
	v_add_u32_e32 v12, s6, v41
	v_mov_b32_e32 v19, v20
	v_add_u32_e32 v20, s6, v43
	v_mov_b32_e32 v29, v30
	v_add_u32_e32 v30, s6, v45
	v_ashrrev_i32_e32 v7, 31, v4
	v_mad_u64_u32 v[4:5], s[22:23], v4, s36, 0
	v_ashrrev_i32_e32 v15, 31, v12
	v_mad_u64_u32 v[12:13], s[22:23], v12, s36, 0
	v_ashrrev_i32_e32 v23, 31, v20
	v_mad_u64_u32 v[20:21], s[22:23], v20, s36, 0
	v_ashrrev_i32_e32 v33, 31, v30
	v_mad_u64_u32 v[30:31], s[22:23], v30, s36, 0
	v_mov_b32_e32 v6, v5
	v_mov_b32_e32 v14, v13
	v_mov_b32_e32 v22, v21
	v_mov_b32_e32 v32, v31
	v_mad_u64_u32 v[6:7], s[22:23], v7, s36, v[6:7]
	v_mad_u64_u32 v[14:15], s[22:23], v15, s36, v[14:15]
	v_mad_u64_u32 v[22:23], s[22:23], v23, s36, v[22:23]
	v_mad_u64_u32 v[32:33], s[22:23], v33, s36, v[32:33]
	v_mov_b32_e32 v5, v6
	v_mov_b32_e32 v13, v14
	v_mov_b32_e32 v21, v22
	v_mov_b32_e32 v31, v32
	v_lshl_add_u64 v[2:3], v[2:3], 2, v[26:27]
	v_lshl_add_u64 v[6:7], v[4:5], 2, v[26:27]
	v_lshl_add_u64 v[10:11], v[10:11], 2, v[26:27]
	v_lshl_add_u64 v[14:15], v[12:13], 2, v[26:27]
	v_lshl_add_u64 v[18:19], v[18:19], 2, v[26:27]
	v_lshl_add_u64 v[22:23], v[20:21], 2, v[26:27]
	v_lshl_add_u64 v[28:29], v[28:29], 2, v[26:27]
	v_lshl_add_u64 v[30:31], v[30:31], 2, v[26:27]
	global_load_dwordx4 v[2:5], v[2:3], off
	s_nop 0
	global_load_dwordx4 v[6:9], v[6:7], off
	s_nop 0
	global_load_dwordx4 v[10:13], v[10:11], off
	s_nop 0
	global_load_dwordx4 v[14:17], v[14:15], off
	s_nop 0
	global_load_dwordx4 v[18:21], v[18:19], off
	s_nop 0
	global_load_dwordx4 v[22:25], v[22:23], off
	s_nop 0
	global_load_dwordx4 v[26:29], v[28:29], off
	s_nop 0
	global_load_dwordx4 v[30:33], v[30:31], off
.LBB0_1994:
	s_add_i32 s30, s30, -1
	s_cmp_eq_u32 s15, 0
	v_add_u32_e32 v66, s4, v46
	v_lshlrev_b32_e32 v35, 1, v66
	s_cselect_b64 vcc, -1, 0
	s_ashr_i32 s15, s14, 31
	v_and_b32_e32 v35, 0xffffffe0, v35
	s_lshl_b64 s[14:15], s[14:15], 1
	v_add3_u32 v67, s1, v48, v35
	s_add_u32 s2, s2, s14
	s_addc_u32 s3, s3, s15
	v_mov_b32_e32 v35, v37
	v_cndmask_b32_e32 v66, v67, v66, vcc
	v_lshl_add_u64 v[70:71], s[2:3], 0, v[34:35]
	v_ashrrev_i32_e32 v69, 31, v66
	v_mad_u64_u32 v[66:67], s[2:3], v66, s26, 0
	v_mov_b32_e32 v68, v67
	ds_read_b32 v35, v47
	ds_read_b32 v74, v47 offset:516
	ds_read_b32 v75, v47 offset:1032
	ds_read_b32 v76, v47 offset:1548
	ds_read_b32 v77, v47 offset:2064
	ds_read_b32 v78, v47 offset:2580
	ds_read_b32 v79, v47 offset:3096
	ds_read_b32 v80, v47 offset:3612
	v_mad_u64_u32 v[68:69], s[2:3], v69, s26, v[68:69]
	v_mov_b32_e32 v67, v68
	v_lshl_add_u64 v[72:73], v[66:67], 1, v[70:71]
	s_waitcnt lgkmcnt(7)
	v_and_b32_sdwa v67, v35, v38 dst_sel:DWORD dst_unused:UNUSED_PAD src0_sel:WORD_1 src1_sel:DWORD
	v_add3_u32 v35, v35, v67, s31
	s_waitcnt lgkmcnt(4)
	v_and_b32_sdwa v67, v76, v38 dst_sel:DWORD dst_unused:UNUSED_PAD src0_sel:WORD_1 src1_sel:DWORD
	v_and_b32_sdwa v68, v74, v38 dst_sel:DWORD dst_unused:UNUSED_PAD src0_sel:WORD_1 src1_sel:DWORD
	v_and_b32_sdwa v66, v75, v38 dst_sel:DWORD dst_unused:UNUSED_PAD src0_sel:WORD_1 src1_sel:DWORD
	v_add3_u32 v67, v76, v67, s31
	v_add3_u32 v68, v74, v68, s31
	v_add3_u32 v66, v75, v66, s31
	v_and_b32_e32 v67, 0xffff0000, v67
	v_and_b32_e32 v68, 0xffff0000, v68
	s_waitcnt lgkmcnt(0)
	v_and_b32_sdwa v69, v80, v38 dst_sel:DWORD dst_unused:UNUSED_PAD src0_sel:WORD_1 src1_sel:DWORD
	v_and_b32_sdwa v74, v78, v38 dst_sel:DWORD dst_unused:UNUSED_PAD src0_sel:WORD_1 src1_sel:DWORD
	v_or_b32_sdwa v67, v67, v66 dst_sel:DWORD dst_unused:UNUSED_PAD src0_sel:DWORD src1_sel:WORD_1
	v_or_b32_sdwa v66, v68, v35 dst_sel:DWORD dst_unused:UNUSED_PAD src0_sel:DWORD src1_sel:WORD_1
	v_and_b32_sdwa v35, v79, v38 dst_sel:DWORD dst_unused:UNUSED_PAD src0_sel:WORD_1 src1_sel:DWORD
	v_and_b32_sdwa v68, v77, v38 dst_sel:DWORD dst_unused:UNUSED_PAD src0_sel:WORD_1 src1_sel:DWORD
	v_add3_u32 v69, v80, v69, s31
	v_add3_u32 v74, v78, v74, s31
	v_add3_u32 v68, v77, v68, s31
	v_add3_u32 v35, v79, v35, s31
	v_and_b32_e32 v69, 0xffff0000, v69
	v_and_b32_e32 v74, 0xffff0000, v74
	v_or_b32_sdwa v69, v69, v35 dst_sel:DWORD dst_unused:UNUSED_PAD src0_sel:DWORD src1_sel:WORD_1
	v_or_b32_sdwa v68, v74, v68 dst_sel:DWORD dst_unused:UNUSED_PAD src0_sel:DWORD src1_sel:WORD_1
	global_store_dwordx4 v[72:73], v[66:69], off
	ds_read_b32 v35, v50
	ds_read_b32 v74, v50 offset:516
	ds_read_b32 v75, v50 offset:1032
	ds_read_b32 v76, v50 offset:1548
	ds_read_b32 v77, v50 offset:2064
	ds_read_b32 v78, v50 offset:2580
	ds_read_b32 v79, v50 offset:3096
	ds_read_b32 v80, v50 offset:3612
	v_add_u32_e32 v66, s4, v49
	v_lshlrev_b32_e32 v67, 1, v66
	v_and_b32_e32 v67, 0xffffffe0, v67
	v_add3_u32 v67, s1, v51, v67
	v_cndmask_b32_e32 v66, v67, v66, vcc
	v_ashrrev_i32_e32 v69, 31, v66
	v_mad_u64_u32 v[66:67], s[2:3], v66, s26, 0
	v_mov_b32_e32 v68, v67
	v_mad_u64_u32 v[68:69], s[2:3], v69, s26, v[68:69]
	v_mov_b32_e32 v67, v68
	v_lshl_add_u64 v[72:73], v[66:67], 1, v[70:71]
	s_waitcnt lgkmcnt(7)
	v_and_b32_sdwa v67, v35, v38 dst_sel:DWORD dst_unused:UNUSED_PAD src0_sel:WORD_1 src1_sel:DWORD
	v_add3_u32 v35, v35, v67, s31
	s_waitcnt lgkmcnt(4)
	v_and_b32_sdwa v67, v76, v38 dst_sel:DWORD dst_unused:UNUSED_PAD src0_sel:WORD_1 src1_sel:DWORD
	v_and_b32_sdwa v68, v74, v38 dst_sel:DWORD dst_unused:UNUSED_PAD src0_sel:WORD_1 src1_sel:DWORD
	v_and_b32_sdwa v66, v75, v38 dst_sel:DWORD dst_unused:UNUSED_PAD src0_sel:WORD_1 src1_sel:DWORD
	v_add3_u32 v67, v76, v67, s31
	v_add3_u32 v68, v74, v68, s31
	v_add3_u32 v66, v75, v66, s31
	v_and_b32_e32 v67, 0xffff0000, v67
	v_and_b32_e32 v68, 0xffff0000, v68
	s_waitcnt lgkmcnt(0)
	v_and_b32_sdwa v69, v80, v38 dst_sel:DWORD dst_unused:UNUSED_PAD src0_sel:WORD_1 src1_sel:DWORD
	v_and_b32_sdwa v74, v78, v38 dst_sel:DWORD dst_unused:UNUSED_PAD src0_sel:WORD_1 src1_sel:DWORD
	v_or_b32_sdwa v67, v67, v66 dst_sel:DWORD dst_unused:UNUSED_PAD src0_sel:DWORD src1_sel:WORD_1
	v_or_b32_sdwa v66, v68, v35 dst_sel:DWORD dst_unused:UNUSED_PAD src0_sel:DWORD src1_sel:WORD_1
	v_and_b32_sdwa v35, v79, v38 dst_sel:DWORD dst_unused:UNUSED_PAD src0_sel:WORD_1 src1_sel:DWORD
	v_and_b32_sdwa v68, v77, v38 dst_sel:DWORD dst_unused:UNUSED_PAD src0_sel:WORD_1 src1_sel:DWORD
	v_add3_u32 v69, v80, v69, s31
	v_add3_u32 v74, v78, v74, s31
	v_add3_u32 v68, v77, v68, s31
	v_add3_u32 v35, v79, v35, s31
	v_and_b32_e32 v69, 0xffff0000, v69
	v_and_b32_e32 v74, 0xffff0000, v74
	v_or_b32_sdwa v69, v69, v35 dst_sel:DWORD dst_unused:UNUSED_PAD src0_sel:DWORD src1_sel:WORD_1
	v_or_b32_sdwa v68, v74, v68 dst_sel:DWORD dst_unused:UNUSED_PAD src0_sel:DWORD src1_sel:WORD_1
	global_store_dwordx4 v[72:73], v[66:69], off
	ds_read_b32 v35, v53
	ds_read_b32 v74, v53 offset:516
	ds_read_b32 v75, v53 offset:1032
	ds_read_b32 v76, v53 offset:1548
	ds_read_b32 v77, v53 offset:2064
	ds_read_b32 v78, v53 offset:2580
	ds_read_b32 v79, v53 offset:3096
	ds_read_b32 v80, v53 offset:3612
	v_add_u32_e32 v66, s4, v52
	v_lshlrev_b32_e32 v67, 1, v66
	v_and_b32_e32 v67, 0xffffffe0, v67
	v_add3_u32 v67, s1, v54, v67
	v_cndmask_b32_e32 v66, v67, v66, vcc
	v_ashrrev_i32_e32 v69, 31, v66
	v_mad_u64_u32 v[66:67], s[2:3], v66, s26, 0
	v_mov_b32_e32 v68, v67
	v_mad_u64_u32 v[68:69], s[2:3], v69, s26, v[68:69]
	v_mov_b32_e32 v67, v68
	v_lshl_add_u64 v[72:73], v[66:67], 1, v[70:71]
	s_waitcnt lgkmcnt(7)
	v_and_b32_sdwa v67, v35, v38 dst_sel:DWORD dst_unused:UNUSED_PAD src0_sel:WORD_1 src1_sel:DWORD
	v_add3_u32 v35, v35, v67, s31
	s_waitcnt lgkmcnt(4)
	v_and_b32_sdwa v67, v76, v38 dst_sel:DWORD dst_unused:UNUSED_PAD src0_sel:WORD_1 src1_sel:DWORD
	v_and_b32_sdwa v68, v74, v38 dst_sel:DWORD dst_unused:UNUSED_PAD src0_sel:WORD_1 src1_sel:DWORD
	v_and_b32_sdwa v66, v75, v38 dst_sel:DWORD dst_unused:UNUSED_PAD src0_sel:WORD_1 src1_sel:DWORD
	v_add3_u32 v67, v76, v67, s31
	v_add3_u32 v68, v74, v68, s31
	v_add3_u32 v66, v75, v66, s31
	v_and_b32_e32 v67, 0xffff0000, v67
	v_and_b32_e32 v68, 0xffff0000, v68
	s_waitcnt lgkmcnt(0)
	v_and_b32_sdwa v69, v80, v38 dst_sel:DWORD dst_unused:UNUSED_PAD src0_sel:WORD_1 src1_sel:DWORD
	v_and_b32_sdwa v74, v78, v38 dst_sel:DWORD dst_unused:UNUSED_PAD src0_sel:WORD_1 src1_sel:DWORD
	v_or_b32_sdwa v67, v67, v66 dst_sel:DWORD dst_unused:UNUSED_PAD src0_sel:DWORD src1_sel:WORD_1
	v_or_b32_sdwa v66, v68, v35 dst_sel:DWORD dst_unused:UNUSED_PAD src0_sel:DWORD src1_sel:WORD_1
	v_and_b32_sdwa v35, v79, v38 dst_sel:DWORD dst_unused:UNUSED_PAD src0_sel:WORD_1 src1_sel:DWORD
	v_and_b32_sdwa v68, v77, v38 dst_sel:DWORD dst_unused:UNUSED_PAD src0_sel:WORD_1 src1_sel:DWORD
	v_add3_u32 v69, v80, v69, s31
	v_add3_u32 v74, v78, v74, s31
	v_add3_u32 v68, v77, v68, s31
	v_add3_u32 v35, v79, v35, s31
	v_and_b32_e32 v69, 0xffff0000, v69
	v_and_b32_e32 v74, 0xffff0000, v74
	v_or_b32_sdwa v69, v69, v35 dst_sel:DWORD dst_unused:UNUSED_PAD src0_sel:DWORD src1_sel:WORD_1
	v_or_b32_sdwa v68, v74, v68 dst_sel:DWORD dst_unused:UNUSED_PAD src0_sel:DWORD src1_sel:WORD_1
	global_store_dwordx4 v[72:73], v[66:69], off
	ds_read_b32 v35, v56
	ds_read_b32 v72, v56 offset:516
	ds_read_b32 v73, v56 offset:1032
	ds_read_b32 v74, v56 offset:1548
	ds_read_b32 v75, v56 offset:2064
	ds_read_b32 v76, v56 offset:2580
	ds_read_b32 v77, v56 offset:3096
	ds_read_b32 v78, v56 offset:3612
	v_add_u32_e32 v66, s4, v55
	v_lshlrev_b32_e32 v67, 1, v66
	v_and_b32_e32 v67, 0xffffffe0, v67
	v_add3_u32 v67, s1, v57, v67
	v_cndmask_b32_e32 v66, v67, v66, vcc
	v_ashrrev_i32_e32 v69, 31, v66
	v_mad_u64_u32 v[66:67], s[2:3], v66, s26, 0
	v_mov_b32_e32 v68, v67
	v_mad_u64_u32 v[68:69], s[2:3], v69, s26, v[68:69]
	v_mov_b32_e32 v67, v68
	v_lshl_add_u64 v[70:71], v[66:67], 1, v[70:71]
	s_waitcnt lgkmcnt(7)
	v_and_b32_sdwa v67, v35, v38 dst_sel:DWORD dst_unused:UNUSED_PAD src0_sel:WORD_1 src1_sel:DWORD
	v_add3_u32 v35, v35, v67, s31
	s_waitcnt lgkmcnt(4)
	v_and_b32_sdwa v67, v74, v38 dst_sel:DWORD dst_unused:UNUSED_PAD src0_sel:WORD_1 src1_sel:DWORD
	v_and_b32_sdwa v68, v72, v38 dst_sel:DWORD dst_unused:UNUSED_PAD src0_sel:WORD_1 src1_sel:DWORD
	v_and_b32_sdwa v66, v73, v38 dst_sel:DWORD dst_unused:UNUSED_PAD src0_sel:WORD_1 src1_sel:DWORD
	v_add3_u32 v67, v74, v67, s31
	v_add3_u32 v68, v72, v68, s31
	v_add3_u32 v66, v73, v66, s31
	v_and_b32_e32 v67, 0xffff0000, v67
	v_and_b32_e32 v68, 0xffff0000, v68
	s_waitcnt lgkmcnt(0)
	v_and_b32_sdwa v69, v78, v38 dst_sel:DWORD dst_unused:UNUSED_PAD src0_sel:WORD_1 src1_sel:DWORD
	v_and_b32_sdwa v72, v76, v38 dst_sel:DWORD dst_unused:UNUSED_PAD src0_sel:WORD_1 src1_sel:DWORD
	v_or_b32_sdwa v67, v67, v66 dst_sel:DWORD dst_unused:UNUSED_PAD src0_sel:DWORD src1_sel:WORD_1
	v_or_b32_sdwa v66, v68, v35 dst_sel:DWORD dst_unused:UNUSED_PAD src0_sel:DWORD src1_sel:WORD_1
	v_and_b32_sdwa v35, v77, v38 dst_sel:DWORD dst_unused:UNUSED_PAD src0_sel:WORD_1 src1_sel:DWORD
	v_and_b32_sdwa v68, v75, v38 dst_sel:DWORD dst_unused:UNUSED_PAD src0_sel:WORD_1 src1_sel:DWORD
	v_add3_u32 v69, v78, v69, s31
	v_add3_u32 v72, v76, v72, s31
	v_add3_u32 v68, v75, v68, s31
	v_add3_u32 v35, v77, v35, s31
	v_and_b32_e32 v69, 0xffff0000, v69
	v_and_b32_e32 v72, 0xffff0000, v72
	v_or_b32_sdwa v69, v69, v35 dst_sel:DWORD dst_unused:UNUSED_PAD src0_sel:DWORD src1_sel:WORD_1
	v_or_b32_sdwa v68, v72, v68 dst_sel:DWORD dst_unused:UNUSED_PAD src0_sel:DWORD src1_sel:WORD_1
	s_add_i32 s29, s29, 1
	s_and_b64 vcc, exec, s[16:17]
	s_mov_b32 s34, s33
	s_mov_b32 s1, s35
	s_mov_b32 s15, s24
	s_mov_b32 s4, s20
	s_mov_b32 s14, s6
	s_mov_b32 s26, s25
	s_mov_b64 s[2:3], s[18:19]
	global_store_dwordx4 v[70:71], v[66:69], off
	s_barrier
	s_cbranch_vccnz .LBB0_2013

.LBB0_2313:
	s_waitcnt vmcnt(11)
	v_add_u32_e32 v2, 0x800, v130
	s_lshr_b32 s0, s12, 7
	v_ashrrev_i32_e32 v41, 5, v2
	v_cvt_f32_u32_e32 v2, s0
	s_sub_i32 s14, 0, s0
	s_abs_i32 s9, s13
	s_ashr_i32 s8, s13, 31
	v_rcp_iflag_f32_e32 v2, v2
	v_add_u32_e32 v3, 0xa00, v130
	v_ashrrev_i32_e32 v42, 5, v3
	v_add_u32_e32 v3, 0xc00, v130
	v_mul_f32_e32 v2, 0x4f7ffffe, v2
	v_cvt_u32_f32_e32 v2, v2
	v_lshlrev_b32_e32 v1, 2, v130
	v_ashrrev_i32_e32 v43, 5, v3
	v_add_u32_e32 v3, 0xe00, v130
	v_readfirstlane_b32 s15, v2
	s_mul_i32 s14, s14, s15
	s_mul_hi_u32 s14, s15, s14
	s_add_i32 s15, s15, s14
	s_mul_hi_u32 s14, s9, s15
	s_mul_i32 s15, s14, s0
	s_sub_i32 s9, s9, s15
	s_add_i32 s15, s14, 1
	s_sub_i32 s16, s9, s0
	s_cmp_ge_u32 s9, s0
	s_cselect_b32 s14, s15, s14
	s_cselect_b32 s9, s16, s9
	s_add_i32 s15, s14, 1
	s_cmp_ge_u32 s9, s0
	s_cselect_b32 s9, s15, s14
	s_xor_b32 s9, s9, s8
	s_sub_i32 s16, s9, s8
	s_mul_i32 s0, s16, s0
	s_sub_i32 s0, s13, s0
	s_lshl_b32 s8, s0, 7
	s_ashr_i32 s9, s8, 31
	s_lshl_b64 s[14:15], s[8:9], 2
	s_add_u32 s10, s10, s14
	v_and_b32_e32 v36, 0x7c, v1
	v_ashrrev_i32_e32 v44, 5, v3
	s_addc_u32 s11, s11, s15
	s_lshl_b32 s20, s16, 7
	v_mov_b32_e32 v35, 0
	v_lshlrev_b32_e32 v34, 2, v36
	v_add_u32_e32 v4, s20, v44
	v_lshl_add_u64 v[2:3], s[10:11], 0, v[34:35]
	s_waitcnt vmcnt(10)
	v_ashrrev_i32_e32 v7, 31, v4
	v_mad_u64_u32 v[4:5], s[10:11], v4, s12, 0
	v_mov_b32_e32 v6, v5
	v_mad_u64_u32 v[6:7], s[10:11], v7, s12, v[6:7]
	v_mov_b32_e32 v5, v6
	v_add_u32_e32 v6, s20, v43
	v_ashrrev_i32_e32 v9, 31, v6
	v_mad_u64_u32 v[6:7], s[10:11], v6, s12, 0
	v_mov_b32_e32 v8, v7
	v_mad_u64_u32 v[8:9], s[10:11], v9, s12, v[8:9]
	v_lshl_add_u64 v[4:5], v[4:5], 2, v[2:3]
	v_mov_b32_e32 v7, v8
	v_lshl_add_u64 v[6:7], v[6:7], 2, v[2:3]
	global_load_dwordx4 v[30:33], v[4:5], off
	global_load_dwordx4 v[26:29], v[6:7], off
	v_add_u32_e32 v4, s20, v42
	v_ashrrev_i32_e32 v7, 31, v4
	v_mad_u64_u32 v[4:5], s[10:11], v4, s12, 0
	v_mov_b32_e32 v6, v5
	v_mad_u64_u32 v[6:7], s[10:11], v7, s12, v[6:7]
	v_mov_b32_e32 v5, v6
	v_add_u32_e32 v6, s20, v41
	v_ashrrev_i32_e32 v9, 31, v6
	v_mad_u64_u32 v[6:7], s[10:11], v6, s12, 0
	v_mov_b32_e32 v8, v7
	v_add_u32_e32 v54, 0x600, v130
	v_mad_u64_u32 v[8:9], s[10:11], v9, s12, v[8:9]
	v_ashrrev_i32_e32 v40, 5, v54
	v_lshl_add_u64 v[4:5], v[4:5], 2, v[2:3]
	v_mov_b32_e32 v7, v8
	v_lshl_add_u64 v[6:7], v[6:7], 2, v[2:3]
	global_load_dwordx4 v[22:25], v[4:5], off
	global_load_dwordx4 v[18:21], v[6:7], off
	v_add_u32_e32 v4, s20, v40
	v_ashrrev_i32_e32 v7, 31, v4
	v_mad_u64_u32 v[4:5], s[10:11], v4, s12, 0
	v_add_u32_e32 v51, 0x400, v130
	v_mov_b32_e32 v6, v5
	v_ashrrev_i32_e32 v39, 5, v51
	v_mad_u64_u32 v[6:7], s[10:11], v7, s12, v[6:7]
	v_mov_b32_e32 v5, v6
	v_add_u32_e32 v6, s20, v39
	v_ashrrev_i32_e32 v9, 31, v6
	v_mad_u64_u32 v[6:7], s[10:11], v6, s12, 0
	v_mov_b32_e32 v8, v7
	v_add_u32_e32 v37, 0x200, v130
	v_mad_u64_u32 v[8:9], s[10:11], v9, s12, v[8:9]
	v_ashrrev_i32_e32 v38, 5, v37
	v_lshl_add_u64 v[4:5], v[4:5], 2, v[2:3]
	v_mov_b32_e32 v7, v8
	v_lshl_add_u64 v[6:7], v[6:7], 2, v[2:3]
	global_load_dwordx4 v[14:17], v[4:5], off
	global_load_dwordx4 v[10:13], v[6:7], off
	v_add_u32_e32 v4, s20, v38
	v_ashrrev_i32_e32 v7, 31, v4
	v_mad_u64_u32 v[4:5], s[10:11], v4, s12, 0
	v_mov_b32_e32 v6, v5
	v_ashrrev_i32_e32 v1, 5, v130
	v_mad_u64_u32 v[6:7], s[10:11], v7, s12, v[6:7]
	v_mov_b32_e32 v5, v6
	v_add_u32_e32 v6, s20, v1
	v_ashrrev_i32_e32 v9, 31, v6
	v_mad_u64_u32 v[6:7], s[10:11], v6, s12, 0
	v_mov_b32_e32 v8, v7
	v_mad_u64_u32 v[8:9], s[10:11], v9, s12, v[8:9]
	v_mov_b32_e32 v7, v8
	v_lshl_add_u64 v[4:5], v[4:5], 2, v[2:3]
	v_lshl_add_u64 v[2:3], v[6:7], 2, v[2:3]
	global_load_dwordx4 v[6:9], v[4:5], off
	s_nop 0
	global_load_dwordx4 v[2:5], v[2:3], off
	v_lshlrev_b32_e32 v45, 3, v130
	v_and_b32_e32 v66, 0x78, v45
	s_movk_i32 s0, 0x204
	v_mad_u32_u24 v55, v66, s0, 0
	v_mul_lo_u32 v57, v1, s0
	v_mul_lo_u32 v58, v38, s0
	v_mul_lo_u32 v59, v39, s0
	v_mul_lo_u32 v60, v40, s0
	v_mul_lo_u32 v61, v41, s0
	v_mul_lo_u32 v62, v42, s0
	v_mul_lo_u32 v63, v43, s0
	v_mul_lo_u32 v64, v44, s0
	s_add_u32 s0, s6, 0x1e940000
	s_addc_u32 s9, s7, 0
	s_add_u32 s12, s6, 0x16940000
	s_addc_u32 s13, s7, 0
	s_add_u32 s14, s78, 0x1000000
	s_addc_u32 s15, s79, 0
	s_add_u32 s16, s6, 0x16140000
	s_addc_u32 s17, s7, 0
	v_readlane_b32 s56, v250, 7
	s_add_u32 s36, s6, 0x15540000
	v_readlane_b32 s70, v250, 21
	v_readlane_b32 s71, v250, 22
	s_addc_u32 s37, s7, 0
	s_mov_b64 s[18:19], s[70:71]
	s_add_u32 s18, s18, 0x6c00000
	s_addc_u32 s19, s19, 0
	s_add_u32 s6, s6, 0x11f40000
	v_add_u32_e32 v34, 0, v34
	v_ashrrev_i32_e32 v45, 4, v130
	v_ashrrev_i32_e32 v48, 4, v37
	v_ashrrev_i32_e32 v51, 4, v51
	v_ashrrev_i32_e32 v54, 4, v54
	s_addc_u32 s7, s7, 0
	s_add_i32 s10, s33, s40
	s_mov_b32 s11, 0
	v_lshl_add_u32 v46, v45, 2, v55
	v_and_b32_e32 v47, 15, v45
	v_lshl_add_u32 v49, v48, 2, v55
	v_and_b32_e32 v50, 15, v48
	v_lshl_add_u32 v52, v51, 2, v55
	v_and_b32_e32 v53, 15, v51
	v_lshl_add_u32 v55, v54, 2, v55
	v_and_b32_e32 v56, 15, v54
	s_add_i32 s38, s10, 0xfffff5c0
	s_add_i32 s39, s10, 0xfffff6c0
	v_add_u32_e32 v57, v34, v57
	v_add_u32_e32 v58, v34, v58
	v_add_u32_e32 v59, v34, v59
	v_add_u32_e32 v60, v34, v60
	v_add_u32_e32 v61, v34, v61
	v_add_u32_e32 v62, v34, v62
	v_add_u32_e32 v63, v34, v63
	v_add_u32_e32 v64, v34, v64
	v_lshlrev_b32_e32 v34, 2, v36
	v_lshlrev_b32_e32 v36, 1, v66
	s_movk_i32 s41, 0x7fff
	v_mov_b32_e32 v65, 1
	s_mov_b32 s10, s21
	s_mov_b32 s42, s35
	s_mov_b64 s[24:25], s[2:3]
	v_readlane_b32 s57, v250, 8
	v_readlane_b32 s58, v250, 9
	v_readlane_b32 s59, v250, 10
	v_readlane_b32 s60, v250, 11
	v_readlane_b32 s61, v250, 12
	v_readlane_b32 s62, v250, 13
	v_readlane_b32 s63, v250, 14
	v_readlane_b32 s64, v250, 15
	v_readlane_b32 s65, v250, 16
	v_readlane_b32 s66, v250, 17
	v_readlane_b32 s67, v250, 18
	v_readlane_b32 s68, v250, 19
	v_readlane_b32 s69, v250, 20
	s_branch .LBB0_2317

.LBB0_2315:
	s_lshr_b32 s26, s44, 7
	v_cvt_f32_u32_e32 v2, s26
	s_sub_i32 s31, 0, s26
	s_abs_i32 s30, s45
	s_ashr_i32 s27, s45, 31
	v_rcp_iflag_f32_e32 v2, v2
	s_nop 0
	v_mul_f32_e32 v2, 0x4f7ffffe, v2
	v_cvt_u32_f32_e32 v2, v2
	s_nop 0
	v_readfirstlane_b32 s46, v2
	s_mul_i32 s31, s31, s46
	s_mul_hi_u32 s31, s46, s31
	s_add_i32 s46, s46, s31
	s_mul_hi_u32 s31, s30, s46
	s_mul_i32 s46, s31, s26
	s_sub_i32 s30, s30, s46
	s_add_i32 s47, s31, 1
	s_sub_i32 s46, s30, s26
	s_cmp_ge_u32 s30, s26
	s_cselect_b32 s31, s47, s31
	s_cselect_b32 s30, s46, s30
	s_add_i32 s46, s31, 1
	s_cmp_ge_u32 s30, s26
	s_cselect_b32 s30, s46, s31
	s_xor_b32 s30, s30, s27
	s_sub_i32 s27, s30, s27
	s_lshl_b32 s30, s27, 7
	s_mul_i32 s27, s27, s26
	s_sub_i32 s26, s45, s27
	s_lshl_b32 s26, s26, 7
	s_ashr_i32 s27, s26, 31
	s_lshl_b64 s[46:47], s[26:27], 2
	s_add_u32 s28, s28, s46
	v_add_u32_e32 v2, s30, v1
	s_addc_u32 s29, s29, s47
	v_add_u32_e32 v10, s30, v39
	v_add_u32_e32 v18, s30, v41
	v_add_u32_e32 v28, s30, v43
	v_ashrrev_i32_e32 v5, 31, v2
	v_lshl_add_u64 v[26:27], s[28:29], 0, v[34:35]
	v_mad_u64_u32 v[2:3], s[28:29], v2, s44, 0
	v_ashrrev_i32_e32 v13, 31, v10
	v_mad_u64_u32 v[10:11], s[28:29], v10, s44, 0
	v_ashrrev_i32_e32 v21, 31, v18
	v_mad_u64_u32 v[18:19], s[28:29], v18, s44, 0
	v_ashrrev_i32_e32 v31, 31, v28
	v_mad_u64_u32 v[28:29], s[28:29], v28, s44, 0
	v_mov_b32_e32 v4, v3
	v_mov_b32_e32 v12, v11
	v_mov_b32_e32 v20, v19
	v_mov_b32_e32 v30, v29
	v_mad_u64_u32 v[4:5], s[28:29], v5, s44, v[4:5]
	v_mad_u64_u32 v[12:13], s[28:29], v13, s44, v[12:13]
	v_mad_u64_u32 v[20:21], s[28:29], v21, s44, v[20:21]
	v_mad_u64_u32 v[30:31], s[28:29], v31, s44, v[30:31]
	v_mov_b32_e32 v3, v4
	v_add_u32_e32 v4, s30, v38
	v_mov_b32_e32 v11, v12
	v_add_u32_e32 v12, s30, v40
	v_mov_b32_e32 v19, v20
	v_add_u32_e32 v20, s30, v42
	v_mov_b32_e32 v29, v30
	v_add_u32_e32 v30, s30, v44
	v_ashrrev_i32_e32 v7, 31, v4
	v_mad_u64_u32 v[4:5], s[28:29], v4, s44, 0
	v_ashrrev_i32_e32 v15, 31, v12
	v_mad_u64_u32 v[12:13], s[28:29], v12, s44, 0
	v_ashrrev_i32_e32 v23, 31, v20
	v_mad_u64_u32 v[20:21], s[28:29], v20, s44, 0
	v_ashrrev_i32_e32 v33, 31, v30
	v_mad_u64_u32 v[30:31], s[28:29], v30, s44, 0
	v_mov_b32_e32 v6, v5
	v_mov_b32_e32 v14, v13
	v_mov_b32_e32 v22, v21
	v_mov_b32_e32 v32, v31
	v_mad_u64_u32 v[6:7], s[28:29], v7, s44, v[6:7]
	v_mad_u64_u32 v[14:15], s[28:29], v15, s44, v[14:15]
	v_mad_u64_u32 v[22:23], s[28:29], v23, s44, v[22:23]
	v_mad_u64_u32 v[32:33], s[28:29], v33, s44, v[32:33]
	v_mov_b32_e32 v5, v6
	v_mov_b32_e32 v13, v14
	v_mov_b32_e32 v21, v22
	v_mov_b32_e32 v31, v32
	v_lshl_add_u64 v[2:3], v[2:3], 2, v[26:27]
	v_lshl_add_u64 v[6:7], v[4:5], 2, v[26:27]
	v_lshl_add_u64 v[10:11], v[10:11], 2, v[26:27]
	v_lshl_add_u64 v[14:15], v[12:13], 2, v[26:27]
	v_lshl_add_u64 v[18:19], v[18:19], 2, v[26:27]
	v_lshl_add_u64 v[22:23], v[20:21], 2, v[26:27]
	v_lshl_add_u64 v[28:29], v[28:29], 2, v[26:27]
	v_lshl_add_u64 v[30:31], v[30:31], 2, v[26:27]
	global_load_dwordx4 v[2:5], v[2:3], off
	s_nop 0
	global_load_dwordx4 v[6:9], v[6:7], off
	s_nop 0
	global_load_dwordx4 v[10:13], v[10:11], off
	s_nop 0
	global_load_dwordx4 v[14:17], v[14:15], off
	s_nop 0
	global_load_dwordx4 v[18:21], v[18:19], off
	s_nop 0
	global_load_dwordx4 v[22:25], v[22:23], off
	s_nop 0
	global_load_dwordx4 v[26:29], v[28:29], off
	s_nop 0
	global_load_dwordx4 v[30:33], v[30:31], off
.LBB0_2316:
	s_add_i32 s34, s34, -1
	s_cmp_eq_u32 s21, 0
	v_add_u32_e32 v66, s8, v45
	v_lshlrev_b32_e32 v37, 1, v66
	s_cselect_b64 vcc, -1, 0
	s_ashr_i32 s21, s20, 31
	v_and_b32_e32 v37, 0xffffffe0, v37
	s_lshl_b64 s[20:21], s[20:21], 1
	v_add3_u32 v67, s1, v47, v37
	s_add_u32 s2, s2, s20
	s_addc_u32 s3, s3, s21
	v_mov_b32_e32 v37, v35
	v_cndmask_b32_e32 v66, v67, v66, vcc
	v_lshl_add_u64 v[70:71], s[2:3], 0, v[36:37]
	v_ashrrev_i32_e32 v69, 31, v66
	v_mad_u64_u32 v[66:67], s[2:3], v66, s35, 0
	v_mov_b32_e32 v68, v67
	ds_read_b32 v37, v46
	ds_read_b32 v74, v46 offset:516
	ds_read_b32 v75, v46 offset:1032
	ds_read_b32 v76, v46 offset:1548
	ds_read_b32 v77, v46 offset:2064
	ds_read_b32 v78, v46 offset:2580
	ds_read_b32 v79, v46 offset:3096
	ds_read_b32 v80, v46 offset:3612
	v_mad_u64_u32 v[68:69], s[2:3], v69, s35, v[68:69]
	v_mov_b32_e32 v67, v68
	v_lshl_add_u64 v[72:73], v[66:67], 1, v[70:71]
	s_waitcnt lgkmcnt(7)
	v_and_b32_sdwa v67, v37, v65 dst_sel:DWORD dst_unused:UNUSED_PAD src0_sel:WORD_1 src1_sel:DWORD
	v_add3_u32 v37, v37, v67, s41
	s_waitcnt lgkmcnt(4)
	v_and_b32_sdwa v67, v76, v65 dst_sel:DWORD dst_unused:UNUSED_PAD src0_sel:WORD_1 src1_sel:DWORD
	v_and_b32_sdwa v68, v74, v65 dst_sel:DWORD dst_unused:UNUSED_PAD src0_sel:WORD_1 src1_sel:DWORD
	v_and_b32_sdwa v66, v75, v65 dst_sel:DWORD dst_unused:UNUSED_PAD src0_sel:WORD_1 src1_sel:DWORD
	v_add3_u32 v67, v76, v67, s41
	v_add3_u32 v68, v74, v68, s41
	v_add3_u32 v66, v75, v66, s41
	v_and_b32_e32 v67, 0xffff0000, v67
	v_and_b32_e32 v68, 0xffff0000, v68
	s_waitcnt lgkmcnt(0)
	v_and_b32_sdwa v69, v80, v65 dst_sel:DWORD dst_unused:UNUSED_PAD src0_sel:WORD_1 src1_sel:DWORD
	v_and_b32_sdwa v74, v78, v65 dst_sel:DWORD dst_unused:UNUSED_PAD src0_sel:WORD_1 src1_sel:DWORD
	v_or_b32_sdwa v67, v67, v66 dst_sel:DWORD dst_unused:UNUSED_PAD src0_sel:DWORD src1_sel:WORD_1
	v_or_b32_sdwa v66, v68, v37 dst_sel:DWORD dst_unused:UNUSED_PAD src0_sel:DWORD src1_sel:WORD_1
	v_and_b32_sdwa v37, v79, v65 dst_sel:DWORD dst_unused:UNUSED_PAD src0_sel:WORD_1 src1_sel:DWORD
	v_and_b32_sdwa v68, v77, v65 dst_sel:DWORD dst_unused:UNUSED_PAD src0_sel:WORD_1 src1_sel:DWORD
	v_add3_u32 v69, v80, v69, s41
	v_add3_u32 v74, v78, v74, s41
	v_add3_u32 v68, v77, v68, s41
	v_add3_u32 v37, v79, v37, s41
	v_and_b32_e32 v69, 0xffff0000, v69
	v_and_b32_e32 v74, 0xffff0000, v74
	v_or_b32_sdwa v69, v69, v37 dst_sel:DWORD dst_unused:UNUSED_PAD src0_sel:DWORD src1_sel:WORD_1
	v_or_b32_sdwa v68, v74, v68 dst_sel:DWORD dst_unused:UNUSED_PAD src0_sel:DWORD src1_sel:WORD_1
	global_store_dwordx4 v[72:73], v[66:69], off
	ds_read_b32 v37, v49
	ds_read_b32 v74, v49 offset:516
	ds_read_b32 v75, v49 offset:1032
	ds_read_b32 v76, v49 offset:1548
	ds_read_b32 v77, v49 offset:2064
	ds_read_b32 v78, v49 offset:2580
	ds_read_b32 v79, v49 offset:3096
	ds_read_b32 v80, v49 offset:3612
	v_add_u32_e32 v66, s8, v48
	v_lshlrev_b32_e32 v67, 1, v66
	v_and_b32_e32 v67, 0xffffffe0, v67
	v_add3_u32 v67, s1, v50, v67
	v_cndmask_b32_e32 v66, v67, v66, vcc
	v_ashrrev_i32_e32 v69, 31, v66
	v_mad_u64_u32 v[66:67], s[2:3], v66, s35, 0
	v_mov_b32_e32 v68, v67
	v_mad_u64_u32 v[68:69], s[2:3], v69, s35, v[68:69]
	v_mov_b32_e32 v67, v68
	v_lshl_add_u64 v[72:73], v[66:67], 1, v[70:71]
	s_waitcnt lgkmcnt(7)
	v_and_b32_sdwa v67, v37, v65 dst_sel:DWORD dst_unused:UNUSED_PAD src0_sel:WORD_1 src1_sel:DWORD
	v_add3_u32 v37, v37, v67, s41
	s_waitcnt lgkmcnt(4)
	v_and_b32_sdwa v67, v76, v65 dst_sel:DWORD dst_unused:UNUSED_PAD src0_sel:WORD_1 src1_sel:DWORD
	v_and_b32_sdwa v68, v74, v65 dst_sel:DWORD dst_unused:UNUSED_PAD src0_sel:WORD_1 src1_sel:DWORD
	v_and_b32_sdwa v66, v75, v65 dst_sel:DWORD dst_unused:UNUSED_PAD src0_sel:WORD_1 src1_sel:DWORD
	v_add3_u32 v67, v76, v67, s41
	v_add3_u32 v68, v74, v68, s41
	v_add3_u32 v66, v75, v66, s41
	v_and_b32_e32 v67, 0xffff0000, v67
	v_and_b32_e32 v68, 0xffff0000, v68
	s_waitcnt lgkmcnt(0)
	v_and_b32_sdwa v69, v80, v65 dst_sel:DWORD dst_unused:UNUSED_PAD src0_sel:WORD_1 src1_sel:DWORD
	v_and_b32_sdwa v74, v78, v65 dst_sel:DWORD dst_unused:UNUSED_PAD src0_sel:WORD_1 src1_sel:DWORD
	v_or_b32_sdwa v67, v67, v66 dst_sel:DWORD dst_unused:UNUSED_PAD src0_sel:DWORD src1_sel:WORD_1
	v_or_b32_sdwa v66, v68, v37 dst_sel:DWORD dst_unused:UNUSED_PAD src0_sel:DWORD src1_sel:WORD_1
	v_and_b32_sdwa v37, v79, v65 dst_sel:DWORD dst_unused:UNUSED_PAD src0_sel:WORD_1 src1_sel:DWORD
	v_and_b32_sdwa v68, v77, v65 dst_sel:DWORD dst_unused:UNUSED_PAD src0_sel:WORD_1 src1_sel:DWORD
	v_add3_u32 v69, v80, v69, s41
	v_add3_u32 v74, v78, v74, s41
	v_add3_u32 v68, v77, v68, s41
	v_add3_u32 v37, v79, v37, s41
	v_and_b32_e32 v69, 0xffff0000, v69
	v_and_b32_e32 v74, 0xffff0000, v74
	v_or_b32_sdwa v69, v69, v37 dst_sel:DWORD dst_unused:UNUSED_PAD src0_sel:DWORD src1_sel:WORD_1
	v_or_b32_sdwa v68, v74, v68 dst_sel:DWORD dst_unused:UNUSED_PAD src0_sel:DWORD src1_sel:WORD_1
	global_store_dwordx4 v[72:73], v[66:69], off
	ds_read_b32 v37, v52
	ds_read_b32 v74, v52 offset:516
	ds_read_b32 v75, v52 offset:1032
	ds_read_b32 v76, v52 offset:1548
	ds_read_b32 v77, v52 offset:2064
	ds_read_b32 v78, v52 offset:2580
	ds_read_b32 v79, v52 offset:3096
	ds_read_b32 v80, v52 offset:3612
	v_add_u32_e32 v66, s8, v51
	v_lshlrev_b32_e32 v67, 1, v66
	v_and_b32_e32 v67, 0xffffffe0, v67
	v_add3_u32 v67, s1, v53, v67
	v_cndmask_b32_e32 v66, v67, v66, vcc
	v_ashrrev_i32_e32 v69, 31, v66
	v_mad_u64_u32 v[66:67], s[2:3], v66, s35, 0
	v_mov_b32_e32 v68, v67
	v_mad_u64_u32 v[68:69], s[2:3], v69, s35, v[68:69]
	v_mov_b32_e32 v67, v68
	v_lshl_add_u64 v[72:73], v[66:67], 1, v[70:71]
	s_waitcnt lgkmcnt(7)
	v_and_b32_sdwa v67, v37, v65 dst_sel:DWORD dst_unused:UNUSED_PAD src0_sel:WORD_1 src1_sel:DWORD
	v_add3_u32 v37, v37, v67, s41
	s_waitcnt lgkmcnt(4)
	v_and_b32_sdwa v67, v76, v65 dst_sel:DWORD dst_unused:UNUSED_PAD src0_sel:WORD_1 src1_sel:DWORD
	v_and_b32_sdwa v68, v74, v65 dst_sel:DWORD dst_unused:UNUSED_PAD src0_sel:WORD_1 src1_sel:DWORD
	v_and_b32_sdwa v66, v75, v65 dst_sel:DWORD dst_unused:UNUSED_PAD src0_sel:WORD_1 src1_sel:DWORD
	v_add3_u32 v67, v76, v67, s41
	v_add3_u32 v68, v74, v68, s41
	v_add3_u32 v66, v75, v66, s41
	v_and_b32_e32 v67, 0xffff0000, v67
	v_and_b32_e32 v68, 0xffff0000, v68
	s_waitcnt lgkmcnt(0)
	v_and_b32_sdwa v69, v80, v65 dst_sel:DWORD dst_unused:UNUSED_PAD src0_sel:WORD_1 src1_sel:DWORD
	v_and_b32_sdwa v74, v78, v65 dst_sel:DWORD dst_unused:UNUSED_PAD src0_sel:WORD_1 src1_sel:DWORD
	v_or_b32_sdwa v67, v67, v66 dst_sel:DWORD dst_unused:UNUSED_PAD src0_sel:DWORD src1_sel:WORD_1
	v_or_b32_sdwa v66, v68, v37 dst_sel:DWORD dst_unused:UNUSED_PAD src0_sel:DWORD src1_sel:WORD_1
	v_and_b32_sdwa v37, v79, v65 dst_sel:DWORD dst_unused:UNUSED_PAD src0_sel:WORD_1 src1_sel:DWORD
	v_and_b32_sdwa v68, v77, v65 dst_sel:DWORD dst_unused:UNUSED_PAD src0_sel:WORD_1 src1_sel:DWORD
	v_add3_u32 v69, v80, v69, s41
	v_add3_u32 v74, v78, v74, s41
	v_add3_u32 v68, v77, v68, s41
	v_add3_u32 v37, v79, v37, s41
	v_and_b32_e32 v69, 0xffff0000, v69
	v_and_b32_e32 v74, 0xffff0000, v74
	v_or_b32_sdwa v69, v69, v37 dst_sel:DWORD dst_unused:UNUSED_PAD src0_sel:DWORD src1_sel:WORD_1
	v_or_b32_sdwa v68, v74, v68 dst_sel:DWORD dst_unused:UNUSED_PAD src0_sel:DWORD src1_sel:WORD_1
	global_store_dwordx4 v[72:73], v[66:69], off
	ds_read_b32 v37, v55
	ds_read_b32 v72, v55 offset:516
	ds_read_b32 v73, v55 offset:1032
	ds_read_b32 v74, v55 offset:1548
	ds_read_b32 v75, v55 offset:2064
	ds_read_b32 v76, v55 offset:2580
	ds_read_b32 v77, v55 offset:3096
	ds_read_b32 v78, v55 offset:3612
	v_add_u32_e32 v66, s8, v54
	v_lshlrev_b32_e32 v67, 1, v66
	v_and_b32_e32 v67, 0xffffffe0, v67
	v_add3_u32 v67, s1, v56, v67
	v_cndmask_b32_e32 v66, v67, v66, vcc
	v_ashrrev_i32_e32 v69, 31, v66
	v_mad_u64_u32 v[66:67], s[2:3], v66, s35, 0
	v_mov_b32_e32 v68, v67
	v_mad_u64_u32 v[68:69], s[2:3], v69, s35, v[68:69]
	v_mov_b32_e32 v67, v68
	v_lshl_add_u64 v[70:71], v[66:67], 1, v[70:71]
	s_waitcnt lgkmcnt(7)
	v_and_b32_sdwa v67, v37, v65 dst_sel:DWORD dst_unused:UNUSED_PAD src0_sel:WORD_1 src1_sel:DWORD
	v_add3_u32 v37, v37, v67, s41
	s_waitcnt lgkmcnt(4)
	v_and_b32_sdwa v67, v74, v65 dst_sel:DWORD dst_unused:UNUSED_PAD src0_sel:WORD_1 src1_sel:DWORD
	v_and_b32_sdwa v68, v72, v65 dst_sel:DWORD dst_unused:UNUSED_PAD src0_sel:WORD_1 src1_sel:DWORD
	v_and_b32_sdwa v66, v73, v65 dst_sel:DWORD dst_unused:UNUSED_PAD src0_sel:WORD_1 src1_sel:DWORD
	v_add3_u32 v67, v74, v67, s41
	v_add3_u32 v68, v72, v68, s41
	v_add3_u32 v66, v73, v66, s41
	v_and_b32_e32 v67, 0xffff0000, v67
	v_and_b32_e32 v68, 0xffff0000, v68
	s_waitcnt lgkmcnt(0)
	v_and_b32_sdwa v69, v78, v65 dst_sel:DWORD dst_unused:UNUSED_PAD src0_sel:WORD_1 src1_sel:DWORD
	v_and_b32_sdwa v72, v76, v65 dst_sel:DWORD dst_unused:UNUSED_PAD src0_sel:WORD_1 src1_sel:DWORD
	v_or_b32_sdwa v67, v67, v66 dst_sel:DWORD dst_unused:UNUSED_PAD src0_sel:DWORD src1_sel:WORD_1
	v_or_b32_sdwa v66, v68, v37 dst_sel:DWORD dst_unused:UNUSED_PAD src0_sel:DWORD src1_sel:WORD_1
	v_and_b32_sdwa v37, v77, v65 dst_sel:DWORD dst_unused:UNUSED_PAD src0_sel:WORD_1 src1_sel:DWORD
	v_and_b32_sdwa v68, v75, v65 dst_sel:DWORD dst_unused:UNUSED_PAD src0_sel:WORD_1 src1_sel:DWORD
	v_add3_u32 v69, v78, v69, s41
	v_add3_u32 v72, v76, v72, s41
	v_add3_u32 v68, v75, v68, s41
	v_add3_u32 v37, v77, v37, s41
	v_and_b32_e32 v69, 0xffff0000, v69
	v_and_b32_e32 v72, 0xffff0000, v72
	v_or_b32_sdwa v69, v69, v37 dst_sel:DWORD dst_unused:UNUSED_PAD src0_sel:DWORD src1_sel:WORD_1
	v_or_b32_sdwa v68, v72, v68 dst_sel:DWORD dst_unused:UNUSED_PAD src0_sel:DWORD src1_sel:WORD_1
	s_add_i32 s38, s38, s40
	s_add_i32 s39, s39, s40
	s_andn2_b64 vcc, exec, s[22:23]
	s_mov_b32 s1, s43
	s_mov_b32 s21, s10
	s_mov_b32 s8, s26
	s_mov_b32 s20, s30
	s_mov_b32 s35, s42
	s_mov_b64 s[2:3], s[24:25]
	global_store_dwordx4 v[70:71], v[66:69], off
	s_barrier
	s_cbranch_vccz .LBB0_2335

.LBB0_3747:
	s_waitcnt vmcnt(5)
	v_add_u32_e32 v2, 0x800, v34
	s_lshr_b32 s4, s8, 7
	v_ashrrev_i32_e32 v42, 5, v2
	v_cvt_f32_u32_e32 v2, s4
	s_sub_i32 s11, 0, s4
	s_abs_i32 s10, s9
	s_ashr_i32 s5, s9, 31
	v_rcp_iflag_f32_e32 v2, v2
	v_add_u32_e32 v3, 0xa00, v34
	v_ashrrev_i32_e32 v43, 5, v3
	v_add_u32_e32 v3, 0xc00, v34
	v_mul_f32_e32 v2, 0x4f7ffffe, v2
	v_cvt_u32_f32_e32 v2, v2
	v_lshlrev_b32_e32 v1, 2, v34
	v_ashrrev_i32_e32 v44, 5, v3
	v_add_u32_e32 v3, 0xe00, v34
	v_readfirstlane_b32 s12, v2
	s_mul_i32 s11, s11, s12
	s_mul_hi_u32 s11, s12, s11
	s_add_i32 s12, s12, s11
	s_mul_hi_u32 s11, s10, s12
	s_mul_i32 s12, s11, s4
	s_sub_i32 s10, s10, s12
	s_add_i32 s12, s11, 1
	s_sub_i32 s13, s10, s4
	s_cmp_ge_u32 s10, s4
	s_cselect_b32 s11, s12, s11
	s_cselect_b32 s10, s13, s10
	s_add_i32 s12, s11, 1
	s_cmp_ge_u32 s10, s4
	s_cselect_b32 s10, s12, s11
	s_xor_b32 s10, s10, s5
	s_sub_i32 s12, s10, s5
	s_mul_i32 s4, s12, s4
	s_sub_i32 s4, s9, s4
	s_lshl_b32 s4, s4, 7
	s_ashr_i32 s5, s4, 31
	s_lshl_b64 s[10:11], s[4:5], 2
	s_add_u32 s6, s6, s10
	v_and_b32_e32 v38, 0x7c, v1
	v_ashrrev_i32_e32 v45, 5, v3
	s_addc_u32 s7, s7, s11
	s_lshl_b32 s18, s12, 7
	v_mov_b32_e32 v37, 0
	v_lshlrev_b32_e32 v36, 2, v38
	v_add_u32_e32 v2, s18, v45
	v_lshl_add_u64 v[26:27], s[6:7], 0, v[36:37]
	v_ashrrev_i32_e32 v5, 31, v2
	v_mad_u64_u32 v[2:3], s[6:7], v2, s8, 0
	v_mov_b32_e32 v4, v3
	v_mad_u64_u32 v[4:5], s[6:7], v5, s8, v[4:5]
	v_mov_b32_e32 v3, v4
	v_lshl_add_u64 v[10:11], v[2:3], 2, v[26:27]
	v_add_u32_e32 v2, s18, v44
	v_ashrrev_i32_e32 v5, 31, v2
	v_mad_u64_u32 v[2:3], s[6:7], v2, s8, 0
	v_mov_b32_e32 v4, v3
	v_mad_u64_u32 v[4:5], s[6:7], v5, s8, v[4:5]
	v_mov_b32_e32 v3, v4
	v_lshl_add_u64 v[12:13], v[2:3], 2, v[26:27]
	global_load_dwordx4 v[6:9], v[10:11], off
	global_load_dwordx4 v[2:5], v[12:13], off
	v_add_u32_e32 v10, s18, v43
	v_ashrrev_i32_e32 v13, 31, v10
	v_mad_u64_u32 v[10:11], s[6:7], v10, s8, 0
	v_mov_b32_e32 v12, v11
	v_mad_u64_u32 v[12:13], s[6:7], v13, s8, v[12:13]
	v_mov_b32_e32 v11, v12
	v_lshl_add_u64 v[18:19], v[10:11], 2, v[26:27]
	v_add_u32_e32 v10, s18, v42
	v_ashrrev_i32_e32 v13, 31, v10
	v_mad_u64_u32 v[10:11], s[6:7], v10, s8, 0
	v_mov_b32_e32 v12, v11
	v_add_u32_e32 v55, 0x600, v34
	v_mad_u64_u32 v[12:13], s[6:7], v13, s8, v[12:13]
	v_ashrrev_i32_e32 v41, 5, v55
	v_mov_b32_e32 v11, v12
	v_lshl_add_u64 v[20:21], v[10:11], 2, v[26:27]
	global_load_dwordx4 v[14:17], v[18:19], off
	global_load_dwordx4 v[10:13], v[20:21], off
	v_add_u32_e32 v18, s18, v41
	v_ashrrev_i32_e32 v21, 31, v18
	v_mad_u64_u32 v[18:19], s[6:7], v18, s8, 0
	v_mov_b32_e32 v20, v19
	v_add_u32_e32 v52, 0x400, v34
	v_mad_u64_u32 v[20:21], s[6:7], v21, s8, v[20:21]
	v_ashrrev_i32_e32 v40, 5, v52
	v_mov_b32_e32 v19, v20
	v_lshl_add_u64 v[28:29], v[18:19], 2, v[26:27]
	v_add_u32_e32 v18, s18, v40
	v_ashrrev_i32_e32 v21, 31, v18
	v_mad_u64_u32 v[18:19], s[6:7], v18, s8, 0
	v_mov_b32_e32 v20, v19
	v_add_u32_e32 v39, 0x200, v34
	v_mad_u64_u32 v[20:21], s[6:7], v21, s8, v[20:21]
	v_ashrrev_i32_e32 v35, 5, v39
	v_mov_b32_e32 v19, v20
	s_waitcnt vmcnt(8)
	v_lshl_add_u64 v[30:31], v[18:19], 2, v[26:27]
	global_load_dwordx4 v[22:25], v[28:29], off
	global_load_dwordx4 v[18:21], v[30:31], off
	v_add_u32_e32 v28, s18, v35
	v_ashrrev_i32_e32 v31, 31, v28
	v_mad_u64_u32 v[28:29], s[6:7], v28, s8, 0
	v_mov_b32_e32 v30, v29
	v_mad_u64_u32 v[30:31], s[6:7], v31, s8, v[30:31]
	v_ashrrev_i32_e32 v1, 5, v34
	v_mov_b32_e32 v29, v30
	v_lshl_add_u64 v[46:47], v[28:29], 2, v[26:27]
	v_add_u32_e32 v28, s18, v1
	v_ashrrev_i32_e32 v31, 31, v28
	v_mad_u64_u32 v[28:29], s[6:7], v28, s8, 0
	v_mov_b32_e32 v30, v29
	v_mad_u64_u32 v[30:31], s[6:7], v31, s8, v[30:31]
	v_mov_b32_e32 v29, v30
	v_lshl_add_u64 v[48:49], v[28:29], 2, v[26:27]
	global_load_dwordx4 v[30:33], v[46:47], off
	global_load_dwordx4 v[26:29], v[48:49], off
	v_lshlrev_b32_e32 v46, 3, v34
	v_and_b32_e32 v66, 0x78, v46
	s_movk_i32 s5, 0x204
	v_readlane_b32 s16, v252, 3
	v_mad_u32_u24 v56, v66, s5, 0
	v_mul_lo_u32 v58, v1, s5
	v_mul_lo_u32 v59, v35, s5
	v_mul_lo_u32 v60, v40, s5
	v_mul_lo_u32 v61, v41, s5
	v_mul_lo_u32 v62, v42, s5
	v_mul_lo_u32 v63, v43, s5
	v_mul_lo_u32 v64, v44, s5
	v_mul_lo_u32 v65, v45, s5
	v_readlane_b32 s17, v252, 4
	s_add_u32 s5, s16, 0x1e940000
	s_addc_u32 s30, s17, 0
	s_add_u32 s8, s16, 0x16940000
	s_addc_u32 s9, s17, 0
	s_add_u32 s10, s78, 0x1000000
	s_addc_u32 s11, s79, 0
	s_add_u32 s12, s16, 0x16140000
	s_addc_u32 s13, s17, 0
	v_readlane_b32 s36, v250, 7
	s_add_u32 s31, s16, 0x15540000
	v_readlane_b32 s50, v250, 21
	v_readlane_b32 s51, v250, 22
	s_addc_u32 s33, s17, 0
	s_mov_b64 s[14:15], s[50:51]
	s_add_u32 s14, s14, 0x6c00000
	s_addc_u32 s15, s15, 0
	v_add_u32_e32 v36, 0, v36
	v_ashrrev_i32_e32 v46, 4, v34
	v_ashrrev_i32_e32 v49, 4, v39
	v_ashrrev_i32_e32 v52, 4, v52
	v_ashrrev_i32_e32 v55, 4, v55
	v_readlane_b32 s38, v250, 9
	s_add_u32 s16, s16, 0x11f40000
	s_mov_b32 s7, 0
	v_lshl_add_u32 v47, v46, 2, v56
	v_and_b32_e32 v48, 15, v46
	v_lshl_add_u32 v50, v49, 2, v56
	v_and_b32_e32 v51, 15, v49
	v_lshl_add_u32 v53, v52, 2, v56
	v_and_b32_e32 v54, 15, v52
	v_lshl_add_u32 v56, v55, 2, v56
	v_and_b32_e32 v57, 15, v55
	s_addc_u32 s17, s17, 0
	s_add_i32 s34, s20, 0x15e1
	s_mov_b32 s35, 17
	v_add_u32_e32 v58, v36, v58
	v_add_u32_e32 v59, v36, v59
	v_add_u32_e32 v60, v36, v60
	v_add_u32_e32 v61, v36, v61
	v_add_u32_e32 v62, v36, v62
	v_add_u32_e32 v63, v36, v63
	v_add_u32_e32 v64, v36, v64
	v_add_u32_e32 v65, v36, v65
	v_lshlrev_b32_e32 v36, 2, v38
	v_lshlrev_b32_e32 v38, 1, v66
	s_movk_i32 s36, 0x7fff
	v_mov_b32_e32 v66, 1
	s_mov_b32 s6, s19
	s_mov_b32 s38, s0
	s_mov_b64 s[22:23], s[2:3]
	v_readlane_b32 s37, v250, 8
	v_readlane_b32 s39, v250, 10
	v_readlane_b32 s40, v250, 11
	v_readlane_b32 s41, v250, 12
	v_readlane_b32 s42, v250, 13
	v_readlane_b32 s43, v250, 14
	v_readlane_b32 s44, v250, 15
	v_readlane_b32 s45, v250, 16
	v_readlane_b32 s46, v250, 17
	v_readlane_b32 s47, v250, 18
	v_readlane_b32 s48, v250, 19
	v_readlane_b32 s49, v250, 20
	s_branch .LBB0_3751

.LBB0_3749:
	s_lshr_b32 s24, s40, 7
	v_cvt_f32_u32_e32 v2, s24
	s_sub_i32 s29, 0, s24
	s_abs_i32 s28, s41
	s_ashr_i32 s25, s41, 31
	v_rcp_iflag_f32_e32 v2, v2
	s_nop 0
	v_mul_f32_e32 v2, 0x4f7ffffe, v2
	v_cvt_u32_f32_e32 v2, v2
	s_nop 0
	v_readfirstlane_b32 s42, v2
	s_mul_i32 s29, s29, s42
	s_mul_hi_u32 s29, s42, s29
	s_add_i32 s42, s42, s29
	s_mul_hi_u32 s29, s28, s42
	s_mul_i32 s42, s29, s24
	s_sub_i32 s28, s28, s42
	s_add_i32 s43, s29, 1
	s_sub_i32 s42, s28, s24
	s_cmp_ge_u32 s28, s24
	s_cselect_b32 s29, s43, s29
	s_cselect_b32 s28, s42, s28
	s_add_i32 s42, s29, 1
	s_cmp_ge_u32 s28, s24
	s_cselect_b32 s28, s42, s29
	s_xor_b32 s28, s28, s25
	s_sub_i32 s25, s28, s25
	s_lshl_b32 s29, s25, 7
	s_mul_i32 s25, s25, s24
	s_sub_i32 s24, s41, s25
	s_lshl_b32 s24, s24, 7
	s_ashr_i32 s25, s24, 31
	s_lshl_b64 s[42:43], s[24:25], 2
	s_add_u32 s26, s26, s42
	v_add_u32_e32 v4, s29, v1
	s_addc_u32 s27, s27, s43
	v_ashrrev_i32_e32 v7, 31, v4
	v_lshl_add_u64 v[2:3], s[26:27], 0, v[36:37]
	v_mad_u64_u32 v[4:5], s[26:27], v4, s40, 0
	v_mov_b32_e32 v6, v5
	v_mad_u64_u32 v[6:7], s[26:27], v7, s40, v[6:7]
	v_mov_b32_e32 v5, v6
	v_add_u32_e32 v6, s29, v35
	v_ashrrev_i32_e32 v9, 31, v6
	v_mad_u64_u32 v[6:7], s[26:27], v6, s40, 0
	v_mov_b32_e32 v8, v7
	v_mad_u64_u32 v[8:9], s[26:27], v9, s40, v[8:9]
	v_lshl_add_u64 v[4:5], v[4:5], 2, v[2:3]
	v_mov_b32_e32 v7, v8
	v_lshl_add_u64 v[6:7], v[6:7], 2, v[2:3]
	global_load_dwordx4 v[26:29], v[4:5], off
	global_load_dwordx4 v[30:33], v[6:7], off
	v_add_u32_e32 v4, s29, v40
	v_ashrrev_i32_e32 v7, 31, v4
	v_mad_u64_u32 v[4:5], s[26:27], v4, s40, 0
	v_mov_b32_e32 v6, v5
	v_mad_u64_u32 v[6:7], s[26:27], v7, s40, v[6:7]
	v_mov_b32_e32 v5, v6
	v_add_u32_e32 v6, s29, v41
	v_ashrrev_i32_e32 v9, 31, v6
	v_mad_u64_u32 v[6:7], s[26:27], v6, s40, 0
	v_mov_b32_e32 v8, v7
	v_mad_u64_u32 v[8:9], s[26:27], v9, s40, v[8:9]
	v_lshl_add_u64 v[4:5], v[4:5], 2, v[2:3]
	v_mov_b32_e32 v7, v8
	v_lshl_add_u64 v[6:7], v[6:7], 2, v[2:3]
	global_load_dwordx4 v[18:21], v[4:5], off
	global_load_dwordx4 v[22:25], v[6:7], off
	v_add_u32_e32 v4, s29, v42
	v_ashrrev_i32_e32 v7, 31, v4
	v_mad_u64_u32 v[4:5], s[26:27], v4, s40, 0
	v_mov_b32_e32 v6, v5
	v_mad_u64_u32 v[6:7], s[26:27], v7, s40, v[6:7]
	v_mov_b32_e32 v5, v6
	v_add_u32_e32 v6, s29, v43
	v_ashrrev_i32_e32 v9, 31, v6
	v_mad_u64_u32 v[6:7], s[26:27], v6, s40, 0
	v_mov_b32_e32 v8, v7
	v_mad_u64_u32 v[8:9], s[26:27], v9, s40, v[8:9]
	v_lshl_add_u64 v[4:5], v[4:5], 2, v[2:3]
	v_mov_b32_e32 v7, v8
	v_lshl_add_u64 v[6:7], v[6:7], 2, v[2:3]
	global_load_dwordx4 v[10:13], v[4:5], off
	global_load_dwordx4 v[14:17], v[6:7], off
	v_add_u32_e32 v4, s29, v44
	v_ashrrev_i32_e32 v7, 31, v4
	v_mad_u64_u32 v[4:5], s[26:27], v4, s40, 0
	v_mov_b32_e32 v6, v5
	v_mad_u64_u32 v[6:7], s[26:27], v7, s40, v[6:7]
	v_mov_b32_e32 v5, v6
	v_add_u32_e32 v6, s29, v45
	v_ashrrev_i32_e32 v9, 31, v6
	v_mad_u64_u32 v[6:7], s[26:27], v6, s40, 0
	v_mov_b32_e32 v8, v7
	v_mad_u64_u32 v[8:9], s[26:27], v9, s40, v[8:9]
	v_mov_b32_e32 v7, v8
	v_lshl_add_u64 v[4:5], v[4:5], 2, v[2:3]
	v_lshl_add_u64 v[6:7], v[6:7], 2, v[2:3]
	global_load_dwordx4 v[2:5], v[4:5], off
	s_nop 0
	global_load_dwordx4 v[6:9], v[6:7], off
.LBB0_3750:
	s_add_i32 s35, s35, -1
	s_cmp_eq_u32 s19, 0
	v_add_u32_e32 v67, s4, v46
	v_lshlrev_b32_e32 v39, 1, v67
	s_cselect_b64 vcc, -1, 0
	s_ashr_i32 s19, s18, 31
	v_and_b32_e32 v39, 0xffffffe0, v39
	s_lshl_b64 s[18:19], s[18:19], 1
	v_add3_u32 v68, s1, v48, v39
	s_add_u32 s2, s2, s18
	s_addc_u32 s3, s3, s19
	v_mov_b32_e32 v39, v37
	v_cndmask_b32_e32 v67, v68, v67, vcc
	v_lshl_add_u64 v[72:73], s[2:3], 0, v[38:39]
	v_mad_u64_u32 v[68:69], s[2:3], v67, s0, 0
	v_ashrrev_i32_e32 v71, 31, v67
	v_mov_b32_e32 v70, v69
	v_mad_u64_u32 v[70:71], s[2:3], v71, s0, v[70:71]
	ds_read_b32 v39, v47
	ds_read_b32 v76, v47 offset:516
	ds_read_b32 v77, v47 offset:1032
	ds_read_b32 v78, v47 offset:1548
	ds_read_b32 v79, v47 offset:2064
	ds_read_b32 v80, v47 offset:2580
	ds_read_b32 v81, v47 offset:3096
	ds_read_b32 v82, v47 offset:3612
	v_mov_b32_e32 v69, v70
	v_lshl_add_u64 v[74:75], v[68:69], 1, v[72:73]
	s_waitcnt lgkmcnt(7)
	v_and_b32_sdwa v68, v39, v66 dst_sel:DWORD dst_unused:UNUSED_PAD src0_sel:WORD_1 src1_sel:DWORD
	v_add3_u32 v39, v39, v68, s36
	s_waitcnt lgkmcnt(4)
	v_and_b32_sdwa v68, v78, v66 dst_sel:DWORD dst_unused:UNUSED_PAD src0_sel:WORD_1 src1_sel:DWORD
	v_and_b32_sdwa v69, v76, v66 dst_sel:DWORD dst_unused:UNUSED_PAD src0_sel:WORD_1 src1_sel:DWORD
	v_and_b32_sdwa v67, v77, v66 dst_sel:DWORD dst_unused:UNUSED_PAD src0_sel:WORD_1 src1_sel:DWORD
	v_add3_u32 v68, v78, v68, s36
	v_add3_u32 v69, v76, v69, s36
	v_add3_u32 v67, v77, v67, s36
	v_and_b32_e32 v68, 0xffff0000, v68
	v_and_b32_e32 v70, 0xffff0000, v69
	v_or_b32_sdwa v69, v68, v67 dst_sel:DWORD dst_unused:UNUSED_PAD src0_sel:DWORD src1_sel:WORD_1
	v_or_b32_sdwa v68, v70, v39 dst_sel:DWORD dst_unused:UNUSED_PAD src0_sel:DWORD src1_sel:WORD_1
	s_waitcnt lgkmcnt(0)
	v_and_b32_sdwa v70, v82, v66 dst_sel:DWORD dst_unused:UNUSED_PAD src0_sel:WORD_1 src1_sel:DWORD
	v_and_b32_sdwa v71, v80, v66 dst_sel:DWORD dst_unused:UNUSED_PAD src0_sel:WORD_1 src1_sel:DWORD
	v_and_b32_sdwa v39, v81, v66 dst_sel:DWORD dst_unused:UNUSED_PAD src0_sel:WORD_1 src1_sel:DWORD
	v_and_b32_sdwa v67, v79, v66 dst_sel:DWORD dst_unused:UNUSED_PAD src0_sel:WORD_1 src1_sel:DWORD
	v_add3_u32 v70, v82, v70, s36
	v_add3_u32 v71, v80, v71, s36
	v_add3_u32 v67, v79, v67, s36
	v_add3_u32 v39, v81, v39, s36
	v_and_b32_e32 v70, 0xffff0000, v70
	v_and_b32_e32 v76, 0xffff0000, v71
	v_or_b32_sdwa v71, v70, v39 dst_sel:DWORD dst_unused:UNUSED_PAD src0_sel:DWORD src1_sel:WORD_1
	v_or_b32_sdwa v70, v76, v67 dst_sel:DWORD dst_unused:UNUSED_PAD src0_sel:DWORD src1_sel:WORD_1
	global_store_dwordx4 v[74:75], v[68:71], off
	ds_read_b32 v39, v50
	ds_read_b32 v67, v50 offset:516
	ds_read_b32 v76, v50 offset:1032
	ds_read_b32 v77, v50 offset:1548
	ds_read_b32 v78, v50 offset:2064
	ds_read_b32 v79, v50 offset:2580
	ds_read_b32 v80, v50 offset:3096
	ds_read_b32 v81, v50 offset:3612
	v_add_u32_e32 v68, s4, v49
	v_lshlrev_b32_e32 v69, 1, v68
	v_and_b32_e32 v69, 0xffffffe0, v69
	v_add3_u32 v69, s1, v51, v69
	v_cndmask_b32_e32 v68, v69, v68, vcc
	v_ashrrev_i32_e32 v71, 31, v68
	v_mad_u64_u32 v[68:69], s[2:3], v68, s0, 0
	v_mov_b32_e32 v70, v69
	v_mad_u64_u32 v[70:71], s[2:3], v71, s0, v[70:71]
	v_mov_b32_e32 v69, v70
	v_lshl_add_u64 v[74:75], v[68:69], 1, v[72:73]
	s_waitcnt lgkmcnt(7)
	v_and_b32_sdwa v69, v39, v66 dst_sel:DWORD dst_unused:UNUSED_PAD src0_sel:WORD_1 src1_sel:DWORD
	v_add3_u32 v39, v39, v69, s36
	s_waitcnt lgkmcnt(4)
	v_and_b32_sdwa v69, v77, v66 dst_sel:DWORD dst_unused:UNUSED_PAD src0_sel:WORD_1 src1_sel:DWORD
	v_and_b32_sdwa v70, v67, v66 dst_sel:DWORD dst_unused:UNUSED_PAD src0_sel:WORD_1 src1_sel:DWORD
	v_and_b32_sdwa v68, v76, v66 dst_sel:DWORD dst_unused:UNUSED_PAD src0_sel:WORD_1 src1_sel:DWORD
	v_add3_u32 v69, v77, v69, s36
	v_add3_u32 v67, v67, v70, s36
	v_add3_u32 v68, v76, v68, s36
	v_and_b32_e32 v69, 0xffff0000, v69
	v_and_b32_e32 v67, 0xffff0000, v67
	s_waitcnt lgkmcnt(0)
	v_and_b32_sdwa v70, v81, v66 dst_sel:DWORD dst_unused:UNUSED_PAD src0_sel:WORD_1 src1_sel:DWORD
	v_and_b32_sdwa v71, v79, v66 dst_sel:DWORD dst_unused:UNUSED_PAD src0_sel:WORD_1 src1_sel:DWORD
	v_or_b32_sdwa v69, v69, v68 dst_sel:DWORD dst_unused:UNUSED_PAD src0_sel:DWORD src1_sel:WORD_1
	v_or_b32_sdwa v68, v67, v39 dst_sel:DWORD dst_unused:UNUSED_PAD src0_sel:DWORD src1_sel:WORD_1
	v_and_b32_sdwa v39, v80, v66 dst_sel:DWORD dst_unused:UNUSED_PAD src0_sel:WORD_1 src1_sel:DWORD
	v_and_b32_sdwa v67, v78, v66 dst_sel:DWORD dst_unused:UNUSED_PAD src0_sel:WORD_1 src1_sel:DWORD
	v_add3_u32 v70, v81, v70, s36
	v_add3_u32 v71, v79, v71, s36
	v_add3_u32 v67, v78, v67, s36
	v_add3_u32 v39, v80, v39, s36
	v_and_b32_e32 v70, 0xffff0000, v70
	v_and_b32_e32 v76, 0xffff0000, v71
	v_or_b32_sdwa v71, v70, v39 dst_sel:DWORD dst_unused:UNUSED_PAD src0_sel:DWORD src1_sel:WORD_1
	v_or_b32_sdwa v70, v76, v67 dst_sel:DWORD dst_unused:UNUSED_PAD src0_sel:DWORD src1_sel:WORD_1
	global_store_dwordx4 v[74:75], v[68:71], off
	ds_read_b32 v39, v53
	ds_read_b32 v67, v53 offset:516
	ds_read_b32 v76, v53 offset:1032
	ds_read_b32 v77, v53 offset:1548
	ds_read_b32 v78, v53 offset:2064
	ds_read_b32 v79, v53 offset:2580
	ds_read_b32 v80, v53 offset:3096
	ds_read_b32 v81, v53 offset:3612
	v_add_u32_e32 v68, s4, v52
	v_lshlrev_b32_e32 v69, 1, v68
	v_and_b32_e32 v69, 0xffffffe0, v69
	v_add3_u32 v69, s1, v54, v69
	v_cndmask_b32_e32 v68, v69, v68, vcc
	v_ashrrev_i32_e32 v71, 31, v68
	v_mad_u64_u32 v[68:69], s[2:3], v68, s0, 0
	v_mov_b32_e32 v70, v69
	v_mad_u64_u32 v[70:71], s[2:3], v71, s0, v[70:71]
	v_mov_b32_e32 v69, v70
	v_lshl_add_u64 v[74:75], v[68:69], 1, v[72:73]
	s_waitcnt lgkmcnt(7)
	v_and_b32_sdwa v69, v39, v66 dst_sel:DWORD dst_unused:UNUSED_PAD src0_sel:WORD_1 src1_sel:DWORD
	v_add3_u32 v39, v39, v69, s36
	s_waitcnt lgkmcnt(4)
	v_and_b32_sdwa v69, v77, v66 dst_sel:DWORD dst_unused:UNUSED_PAD src0_sel:WORD_1 src1_sel:DWORD
	v_and_b32_sdwa v70, v67, v66 dst_sel:DWORD dst_unused:UNUSED_PAD src0_sel:WORD_1 src1_sel:DWORD
	v_and_b32_sdwa v68, v76, v66 dst_sel:DWORD dst_unused:UNUSED_PAD src0_sel:WORD_1 src1_sel:DWORD
	v_add3_u32 v69, v77, v69, s36
	v_add3_u32 v67, v67, v70, s36
	v_add3_u32 v68, v76, v68, s36
	v_and_b32_e32 v69, 0xffff0000, v69
	v_and_b32_e32 v67, 0xffff0000, v67
	s_waitcnt lgkmcnt(0)
	v_and_b32_sdwa v70, v81, v66 dst_sel:DWORD dst_unused:UNUSED_PAD src0_sel:WORD_1 src1_sel:DWORD
	v_and_b32_sdwa v71, v79, v66 dst_sel:DWORD dst_unused:UNUSED_PAD src0_sel:WORD_1 src1_sel:DWORD
	v_or_b32_sdwa v69, v69, v68 dst_sel:DWORD dst_unused:UNUSED_PAD src0_sel:DWORD src1_sel:WORD_1
	v_or_b32_sdwa v68, v67, v39 dst_sel:DWORD dst_unused:UNUSED_PAD src0_sel:DWORD src1_sel:WORD_1
	v_and_b32_sdwa v39, v80, v66 dst_sel:DWORD dst_unused:UNUSED_PAD src0_sel:WORD_1 src1_sel:DWORD
	v_and_b32_sdwa v67, v78, v66 dst_sel:DWORD dst_unused:UNUSED_PAD src0_sel:WORD_1 src1_sel:DWORD
	v_add3_u32 v70, v81, v70, s36
	v_add3_u32 v71, v79, v71, s36
	v_add3_u32 v67, v78, v67, s36
	v_add3_u32 v39, v80, v39, s36
	v_and_b32_e32 v70, 0xffff0000, v70
	v_and_b32_e32 v76, 0xffff0000, v71
	v_or_b32_sdwa v71, v70, v39 dst_sel:DWORD dst_unused:UNUSED_PAD src0_sel:DWORD src1_sel:WORD_1
	v_or_b32_sdwa v70, v76, v67 dst_sel:DWORD dst_unused:UNUSED_PAD src0_sel:DWORD src1_sel:WORD_1
	global_store_dwordx4 v[74:75], v[68:71], off
	ds_read_b32 v39, v56
	ds_read_b32 v67, v56 offset:516
	ds_read_b32 v74, v56 offset:1032
	ds_read_b32 v75, v56 offset:1548
	ds_read_b32 v76, v56 offset:2064
	ds_read_b32 v77, v56 offset:2580
	ds_read_b32 v78, v56 offset:3096
	ds_read_b32 v79, v56 offset:3612
	v_add_u32_e32 v68, s4, v55
	v_lshlrev_b32_e32 v69, 1, v68
	v_and_b32_e32 v69, 0xffffffe0, v69
	v_add3_u32 v69, s1, v57, v69
	v_cndmask_b32_e32 v68, v69, v68, vcc
	v_ashrrev_i32_e32 v71, 31, v68
	v_mad_u64_u32 v[68:69], s[2:3], v68, s0, 0
	v_mov_b32_e32 v70, v69
	v_mad_u64_u32 v[70:71], s[0:1], v71, s0, v[70:71]
	v_mov_b32_e32 v69, v70
	v_lshl_add_u64 v[72:73], v[68:69], 1, v[72:73]
	s_waitcnt lgkmcnt(7)
	v_and_b32_sdwa v69, v39, v66 dst_sel:DWORD dst_unused:UNUSED_PAD src0_sel:WORD_1 src1_sel:DWORD
	v_add3_u32 v39, v39, v69, s36
	s_waitcnt lgkmcnt(4)
	v_and_b32_sdwa v69, v75, v66 dst_sel:DWORD dst_unused:UNUSED_PAD src0_sel:WORD_1 src1_sel:DWORD
	v_and_b32_sdwa v70, v67, v66 dst_sel:DWORD dst_unused:UNUSED_PAD src0_sel:WORD_1 src1_sel:DWORD
	v_and_b32_sdwa v68, v74, v66 dst_sel:DWORD dst_unused:UNUSED_PAD src0_sel:WORD_1 src1_sel:DWORD
	v_add3_u32 v69, v75, v69, s36
	v_add3_u32 v67, v67, v70, s36
	v_add3_u32 v68, v74, v68, s36
	v_and_b32_e32 v69, 0xffff0000, v69
	v_and_b32_e32 v67, 0xffff0000, v67
	s_waitcnt lgkmcnt(0)
	v_and_b32_sdwa v70, v79, v66 dst_sel:DWORD dst_unused:UNUSED_PAD src0_sel:WORD_1 src1_sel:DWORD
	v_and_b32_sdwa v71, v77, v66 dst_sel:DWORD dst_unused:UNUSED_PAD src0_sel:WORD_1 src1_sel:DWORD
	v_or_b32_sdwa v69, v69, v68 dst_sel:DWORD dst_unused:UNUSED_PAD src0_sel:DWORD src1_sel:WORD_1
	v_or_b32_sdwa v68, v67, v39 dst_sel:DWORD dst_unused:UNUSED_PAD src0_sel:DWORD src1_sel:WORD_1
	v_and_b32_sdwa v39, v78, v66 dst_sel:DWORD dst_unused:UNUSED_PAD src0_sel:WORD_1 src1_sel:DWORD
	v_and_b32_sdwa v67, v76, v66 dst_sel:DWORD dst_unused:UNUSED_PAD src0_sel:WORD_1 src1_sel:DWORD
	v_add3_u32 v70, v79, v70, s36
	v_add3_u32 v71, v77, v71, s36
	v_add3_u32 v67, v76, v67, s36
	v_add3_u32 v39, v78, v39, s36
	v_and_b32_e32 v70, 0xffff0000, v70
	v_and_b32_e32 v74, 0xffff0000, v71
	v_or_b32_sdwa v71, v70, v39 dst_sel:DWORD dst_unused:UNUSED_PAD src0_sel:DWORD src1_sel:WORD_1
	v_or_b32_sdwa v70, v74, v67 dst_sel:DWORD dst_unused:UNUSED_PAD src0_sel:DWORD src1_sel:WORD_1
	s_add_i32 s34, s34, 1
	s_and_b64 vcc, exec, s[20:21]
	s_mov_b32 s28, s37
	s_mov_b32 s1, s39
	s_mov_b32 s19, s6
	s_mov_b32 s4, s24
	s_mov_b32 s18, s29
	s_mov_b32 s0, s38
	s_mov_b64 s[2:3], s[22:23]
	global_store_dwordx4 v[72:73], v[68:71], off
	s_barrier
	s_cbranch_vccnz .LBB0_3769

.LBB0_3796:
	s_waitcnt vmcnt(5)
	v_add_u32_e32 v2, 0x800, v34
	s_lshr_b32 s0, s8, 7
	v_ashrrev_i32_e32 v42, 5, v2
	v_cvt_f32_u32_e32 v2, s0
	s_sub_i32 s10, 0, s0
	s_abs_i32 s5, s9
	s_ashr_i32 s4, s9, 31
	v_rcp_iflag_f32_e32 v2, v2
	v_add_u32_e32 v3, 0xa00, v34
	v_ashrrev_i32_e32 v43, 5, v3
	v_add_u32_e32 v3, 0xc00, v34
	v_mul_f32_e32 v2, 0x4f7ffffe, v2
	v_cvt_u32_f32_e32 v2, v2
	v_lshlrev_b32_e32 v1, 2, v34
	v_ashrrev_i32_e32 v44, 5, v3
	v_add_u32_e32 v3, 0xe00, v34
	v_readfirstlane_b32 s11, v2
	s_mul_i32 s10, s10, s11
	s_mul_hi_u32 s10, s11, s10
	s_add_i32 s11, s11, s10
	s_mul_hi_u32 s10, s5, s11
	s_mul_i32 s11, s10, s0
	s_sub_i32 s5, s5, s11
	s_add_i32 s11, s10, 1
	s_sub_i32 s12, s5, s0
	s_cmp_ge_u32 s5, s0
	s_cselect_b32 s10, s11, s10
	s_cselect_b32 s5, s12, s5
	s_add_i32 s11, s10, 1
	s_cmp_ge_u32 s5, s0
	s_cselect_b32 s5, s11, s10
	s_xor_b32 s5, s5, s4
	s_sub_i32 s12, s5, s4
	s_mul_i32 s0, s12, s0
	s_sub_i32 s0, s9, s0
	s_lshl_b32 s4, s0, 7
	s_ashr_i32 s5, s4, 31
	s_lshl_b64 s[10:11], s[4:5], 2
	s_add_u32 s6, s6, s10
	v_and_b32_e32 v38, 0x7c, v1
	v_ashrrev_i32_e32 v45, 5, v3
	s_addc_u32 s7, s7, s11
	s_lshl_b32 s18, s12, 7
	v_mov_b32_e32 v37, 0
	v_lshlrev_b32_e32 v36, 2, v38
	v_add_u32_e32 v2, s18, v45
	v_lshl_add_u64 v[26:27], s[6:7], 0, v[36:37]
	v_ashrrev_i32_e32 v5, 31, v2
	v_mad_u64_u32 v[2:3], s[6:7], v2, s8, 0
	v_mov_b32_e32 v4, v3
	v_mad_u64_u32 v[4:5], s[6:7], v5, s8, v[4:5]
	v_mov_b32_e32 v3, v4
	v_lshl_add_u64 v[10:11], v[2:3], 2, v[26:27]
	v_add_u32_e32 v2, s18, v44
	v_ashrrev_i32_e32 v5, 31, v2
	v_mad_u64_u32 v[2:3], s[6:7], v2, s8, 0
	v_mov_b32_e32 v4, v3
	v_mad_u64_u32 v[4:5], s[6:7], v5, s8, v[4:5]
	v_mov_b32_e32 v3, v4
	v_lshl_add_u64 v[12:13], v[2:3], 2, v[26:27]
	global_load_dwordx4 v[6:9], v[10:11], off
	global_load_dwordx4 v[2:5], v[12:13], off
	v_add_u32_e32 v10, s18, v43
	v_ashrrev_i32_e32 v13, 31, v10
	v_mad_u64_u32 v[10:11], s[6:7], v10, s8, 0
	v_mov_b32_e32 v12, v11
	v_mad_u64_u32 v[12:13], s[6:7], v13, s8, v[12:13]
	v_mov_b32_e32 v11, v12
	v_lshl_add_u64 v[18:19], v[10:11], 2, v[26:27]
	v_add_u32_e32 v10, s18, v42
	v_ashrrev_i32_e32 v13, 31, v10
	v_mad_u64_u32 v[10:11], s[6:7], v10, s8, 0
	v_mov_b32_e32 v12, v11
	v_add_u32_e32 v55, 0x600, v34
	v_mad_u64_u32 v[12:13], s[6:7], v13, s8, v[12:13]
	v_ashrrev_i32_e32 v41, 5, v55
	v_mov_b32_e32 v11, v12
	v_lshl_add_u64 v[20:21], v[10:11], 2, v[26:27]
	global_load_dwordx4 v[14:17], v[18:19], off
	global_load_dwordx4 v[10:13], v[20:21], off
	v_add_u32_e32 v18, s18, v41
	v_ashrrev_i32_e32 v21, 31, v18
	v_mad_u64_u32 v[18:19], s[6:7], v18, s8, 0
	v_mov_b32_e32 v20, v19
	v_add_u32_e32 v52, 0x400, v34
	v_mad_u64_u32 v[20:21], s[6:7], v21, s8, v[20:21]
	v_ashrrev_i32_e32 v40, 5, v52
	v_mov_b32_e32 v19, v20
	v_lshl_add_u64 v[28:29], v[18:19], 2, v[26:27]
	v_add_u32_e32 v18, s18, v40
	v_ashrrev_i32_e32 v21, 31, v18
	v_mad_u64_u32 v[18:19], s[6:7], v18, s8, 0
	v_mov_b32_e32 v20, v19
	v_add_u32_e32 v35, 0x200, v34
	v_mad_u64_u32 v[20:21], s[6:7], v21, s8, v[20:21]
	v_ashrrev_i32_e32 v39, 5, v35
	v_mov_b32_e32 v19, v20
	s_waitcnt vmcnt(8)
	v_lshl_add_u64 v[30:31], v[18:19], 2, v[26:27]
	global_load_dwordx4 v[22:25], v[28:29], off
	global_load_dwordx4 v[18:21], v[30:31], off
	v_add_u32_e32 v28, s18, v39
	v_ashrrev_i32_e32 v31, 31, v28
	v_mad_u64_u32 v[28:29], s[6:7], v28, s8, 0
	v_mov_b32_e32 v30, v29
	v_mad_u64_u32 v[30:31], s[6:7], v31, s8, v[30:31]
	v_ashrrev_i32_e32 v1, 5, v34
	v_mov_b32_e32 v29, v30
	v_lshl_add_u64 v[46:47], v[28:29], 2, v[26:27]
	v_add_u32_e32 v28, s18, v1
	v_ashrrev_i32_e32 v31, 31, v28
	v_mad_u64_u32 v[28:29], s[6:7], v28, s8, 0
	v_mov_b32_e32 v30, v29
	v_mad_u64_u32 v[30:31], s[6:7], v31, s8, v[30:31]
	v_mov_b32_e32 v29, v30
	v_lshl_add_u64 v[48:49], v[28:29], 2, v[26:27]
	global_load_dwordx4 v[30:33], v[46:47], off
	global_load_dwordx4 v[26:29], v[48:49], off
	v_lshlrev_b32_e32 v46, 3, v34
	v_and_b32_e32 v66, 0x78, v46
	s_movk_i32 s0, 0x204
	v_readlane_b32 s16, v252, 3
	v_mad_u32_u24 v56, v66, s0, 0
	v_mul_lo_u32 v58, v1, s0
	v_mul_lo_u32 v59, v39, s0
	v_mul_lo_u32 v60, v40, s0
	v_mul_lo_u32 v61, v41, s0
	v_mul_lo_u32 v62, v42, s0
	v_mul_lo_u32 v63, v43, s0
	v_mul_lo_u32 v64, v44, s0
	v_mul_lo_u32 v65, v45, s0
	v_readlane_b32 s17, v252, 4
	s_add_u32 s0, s16, 0x1e940000
	s_addc_u32 s5, s17, 0
	s_add_u32 s8, s16, 0x16940000
	s_addc_u32 s9, s17, 0
	s_add_u32 s10, s78, 0x1000000
	s_addc_u32 s11, s79, 0
	s_add_u32 s12, s16, 0x16140000
	s_addc_u32 s13, s17, 0
	v_readlane_b32 s36, v250, 7
	s_add_u32 s31, s16, 0x15540000
	v_readlane_b32 s50, v250, 21
	v_readlane_b32 s51, v250, 22
	s_addc_u32 s33, s17, 0
	s_mov_b64 s[14:15], s[50:51]
	s_add_u32 s14, s14, 0x6c00000
	s_addc_u32 s15, s15, 0
	v_add_u32_e32 v36, 0, v36
	v_ashrrev_i32_e32 v46, 4, v34
	v_ashrrev_i32_e32 v49, 4, v35
	v_ashrrev_i32_e32 v52, 4, v52
	v_ashrrev_i32_e32 v55, 4, v55
	v_readlane_b32 s38, v250, 9
	s_add_u32 s16, s16, 0x11f40000
	s_mov_b32 s7, 0
	v_lshl_add_u32 v47, v46, 2, v56
	v_and_b32_e32 v48, 15, v46
	v_lshl_add_u32 v50, v49, 2, v56
	v_and_b32_e32 v51, 15, v49
	v_lshl_add_u32 v53, v52, 2, v56
	v_and_b32_e32 v54, 15, v52
	v_lshl_add_u32 v56, v55, 2, v56
	v_and_b32_e32 v57, 15, v55
	s_addc_u32 s17, s17, 0
	s_add_i32 s34, s20, 0xfffffce1
	s_mov_b32 s35, 25
	v_add_u32_e32 v58, v36, v58
	v_add_u32_e32 v59, v36, v59
	v_add_u32_e32 v60, v36, v60
	v_add_u32_e32 v61, v36, v61
	v_add_u32_e32 v62, v36, v62
	v_add_u32_e32 v63, v36, v63
	v_add_u32_e32 v64, v36, v64
	v_add_u32_e32 v65, v36, v65
	v_lshlrev_b32_e32 v36, 2, v38
	v_lshlrev_b32_e32 v34, 1, v66
	s_movk_i32 s36, 0x7fff
	v_mov_b32_e32 v38, 1
	s_mov_b32 s6, s19
	s_mov_b32 s38, s30
	s_mov_b64 s[22:23], s[2:3]
	v_readlane_b32 s37, v250, 8
	v_readlane_b32 s39, v250, 10
	v_readlane_b32 s40, v250, 11
	v_readlane_b32 s41, v250, 12
	v_readlane_b32 s42, v250, 13
	v_readlane_b32 s43, v250, 14
	v_readlane_b32 s44, v250, 15
	v_readlane_b32 s45, v250, 16
	v_readlane_b32 s46, v250, 17
	v_readlane_b32 s47, v250, 18
	v_readlane_b32 s48, v250, 19
	v_readlane_b32 s49, v250, 20
	s_branch .LBB0_3800

.LBB0_3798:
	s_lshr_b32 s24, s40, 7
	v_cvt_f32_u32_e32 v2, s24
	s_sub_i32 s29, 0, s24
	s_abs_i32 s28, s41
	s_ashr_i32 s25, s41, 31
	v_rcp_iflag_f32_e32 v2, v2
	s_nop 0
	v_mul_f32_e32 v2, 0x4f7ffffe, v2
	v_cvt_u32_f32_e32 v2, v2
	s_nop 0
	v_readfirstlane_b32 s42, v2
	s_mul_i32 s29, s29, s42
	s_mul_hi_u32 s29, s42, s29
	s_add_i32 s42, s42, s29
	s_mul_hi_u32 s29, s28, s42
	s_mul_i32 s42, s29, s24
	s_sub_i32 s28, s28, s42
	s_add_i32 s43, s29, 1
	s_sub_i32 s42, s28, s24
	s_cmp_ge_u32 s28, s24
	s_cselect_b32 s29, s43, s29
	s_cselect_b32 s28, s42, s28
	s_add_i32 s42, s29, 1
	s_cmp_ge_u32 s28, s24
	s_cselect_b32 s28, s42, s29
	s_xor_b32 s28, s28, s25
	s_sub_i32 s25, s28, s25
	s_lshl_b32 s29, s25, 7
	s_mul_i32 s25, s25, s24
	s_sub_i32 s24, s41, s25
	s_lshl_b32 s24, s24, 7
	s_ashr_i32 s25, s24, 31
	s_lshl_b64 s[42:43], s[24:25], 2
	s_add_u32 s26, s26, s42
	v_add_u32_e32 v4, s29, v1
	s_addc_u32 s27, s27, s43
	v_ashrrev_i32_e32 v7, 31, v4
	v_lshl_add_u64 v[2:3], s[26:27], 0, v[36:37]
	v_mad_u64_u32 v[4:5], s[26:27], v4, s40, 0
	v_mov_b32_e32 v6, v5
	v_mad_u64_u32 v[6:7], s[26:27], v7, s40, v[6:7]
	v_mov_b32_e32 v5, v6
	v_add_u32_e32 v6, s29, v39
	v_ashrrev_i32_e32 v9, 31, v6
	v_mad_u64_u32 v[6:7], s[26:27], v6, s40, 0
	v_mov_b32_e32 v8, v7
	v_mad_u64_u32 v[8:9], s[26:27], v9, s40, v[8:9]
	v_lshl_add_u64 v[4:5], v[4:5], 2, v[2:3]
	v_mov_b32_e32 v7, v8
	v_lshl_add_u64 v[6:7], v[6:7], 2, v[2:3]
	global_load_dwordx4 v[26:29], v[4:5], off
	global_load_dwordx4 v[30:33], v[6:7], off
	v_add_u32_e32 v4, s29, v40
	v_ashrrev_i32_e32 v7, 31, v4
	v_mad_u64_u32 v[4:5], s[26:27], v4, s40, 0
	v_mov_b32_e32 v6, v5
	v_mad_u64_u32 v[6:7], s[26:27], v7, s40, v[6:7]
	v_mov_b32_e32 v5, v6
	v_add_u32_e32 v6, s29, v41
	v_ashrrev_i32_e32 v9, 31, v6
	v_mad_u64_u32 v[6:7], s[26:27], v6, s40, 0
	v_mov_b32_e32 v8, v7
	v_mad_u64_u32 v[8:9], s[26:27], v9, s40, v[8:9]
	v_lshl_add_u64 v[4:5], v[4:5], 2, v[2:3]
	v_mov_b32_e32 v7, v8
	v_lshl_add_u64 v[6:7], v[6:7], 2, v[2:3]
	global_load_dwordx4 v[18:21], v[4:5], off
	global_load_dwordx4 v[22:25], v[6:7], off
	v_add_u32_e32 v4, s29, v42
	v_ashrrev_i32_e32 v7, 31, v4
	v_mad_u64_u32 v[4:5], s[26:27], v4, s40, 0
	v_mov_b32_e32 v6, v5
	v_mad_u64_u32 v[6:7], s[26:27], v7, s40, v[6:7]
	v_mov_b32_e32 v5, v6
	v_add_u32_e32 v6, s29, v43
	v_ashrrev_i32_e32 v9, 31, v6
	v_mad_u64_u32 v[6:7], s[26:27], v6, s40, 0
	v_mov_b32_e32 v8, v7
	v_mad_u64_u32 v[8:9], s[26:27], v9, s40, v[8:9]
	v_lshl_add_u64 v[4:5], v[4:5], 2, v[2:3]
	v_mov_b32_e32 v7, v8
	v_lshl_add_u64 v[6:7], v[6:7], 2, v[2:3]
	global_load_dwordx4 v[10:13], v[4:5], off
	global_load_dwordx4 v[14:17], v[6:7], off
	v_add_u32_e32 v4, s29, v44
	v_ashrrev_i32_e32 v7, 31, v4
	v_mad_u64_u32 v[4:5], s[26:27], v4, s40, 0
	v_mov_b32_e32 v6, v5
	v_mad_u64_u32 v[6:7], s[26:27], v7, s40, v[6:7]
	v_mov_b32_e32 v5, v6
	v_add_u32_e32 v6, s29, v45
	v_ashrrev_i32_e32 v9, 31, v6
	v_mad_u64_u32 v[6:7], s[26:27], v6, s40, 0
	v_mov_b32_e32 v8, v7
	v_mad_u64_u32 v[8:9], s[26:27], v9, s40, v[8:9]
	v_mov_b32_e32 v7, v8
	v_lshl_add_u64 v[4:5], v[4:5], 2, v[2:3]
	v_lshl_add_u64 v[6:7], v[6:7], 2, v[2:3]
	global_load_dwordx4 v[2:5], v[4:5], off
	s_nop 0
	global_load_dwordx4 v[6:9], v[6:7], off
.LBB0_3799:
	s_add_i32 s35, s35, -1
	s_cmp_eq_u32 s19, 0
	v_add_u32_e32 v66, s4, v46
	v_lshlrev_b32_e32 v35, 1, v66
	s_cselect_b64 vcc, -1, 0
	s_ashr_i32 s19, s18, 31
	v_and_b32_e32 v35, 0xffffffe0, v35
	s_lshl_b64 s[18:19], s[18:19], 1
	v_add3_u32 v67, s1, v48, v35
	s_add_u32 s2, s2, s18
	s_addc_u32 s3, s3, s19
	v_mov_b32_e32 v35, v37
	v_cndmask_b32_e32 v66, v67, v66, vcc
	v_lshl_add_u64 v[70:71], s[2:3], 0, v[34:35]
	v_ashrrev_i32_e32 v69, 31, v66
	v_mad_u64_u32 v[66:67], s[2:3], v66, s30, 0
	v_mov_b32_e32 v68, v67
	ds_read_b32 v35, v47
	ds_read_b32 v74, v47 offset:516
	ds_read_b32 v75, v47 offset:1032
	ds_read_b32 v76, v47 offset:1548
	ds_read_b32 v77, v47 offset:2064
	ds_read_b32 v78, v47 offset:2580
	ds_read_b32 v79, v47 offset:3096
	ds_read_b32 v80, v47 offset:3612
	v_mad_u64_u32 v[68:69], s[2:3], v69, s30, v[68:69]
	v_mov_b32_e32 v67, v68
	v_lshl_add_u64 v[72:73], v[66:67], 1, v[70:71]
	s_waitcnt lgkmcnt(7)
	v_and_b32_sdwa v67, v35, v38 dst_sel:DWORD dst_unused:UNUSED_PAD src0_sel:WORD_1 src1_sel:DWORD
	v_add3_u32 v35, v35, v67, s36
	s_waitcnt lgkmcnt(4)
	v_and_b32_sdwa v67, v76, v38 dst_sel:DWORD dst_unused:UNUSED_PAD src0_sel:WORD_1 src1_sel:DWORD
	v_and_b32_sdwa v68, v74, v38 dst_sel:DWORD dst_unused:UNUSED_PAD src0_sel:WORD_1 src1_sel:DWORD
	v_and_b32_sdwa v66, v75, v38 dst_sel:DWORD dst_unused:UNUSED_PAD src0_sel:WORD_1 src1_sel:DWORD
	v_add3_u32 v67, v76, v67, s36
	v_add3_u32 v68, v74, v68, s36
	v_add3_u32 v66, v75, v66, s36
	v_and_b32_e32 v67, 0xffff0000, v67
	v_and_b32_e32 v68, 0xffff0000, v68
	s_waitcnt lgkmcnt(0)
	v_and_b32_sdwa v69, v80, v38 dst_sel:DWORD dst_unused:UNUSED_PAD src0_sel:WORD_1 src1_sel:DWORD
	v_and_b32_sdwa v74, v78, v38 dst_sel:DWORD dst_unused:UNUSED_PAD src0_sel:WORD_1 src1_sel:DWORD
	v_or_b32_sdwa v67, v67, v66 dst_sel:DWORD dst_unused:UNUSED_PAD src0_sel:DWORD src1_sel:WORD_1
	v_or_b32_sdwa v66, v68, v35 dst_sel:DWORD dst_unused:UNUSED_PAD src0_sel:DWORD src1_sel:WORD_1
	v_and_b32_sdwa v35, v79, v38 dst_sel:DWORD dst_unused:UNUSED_PAD src0_sel:WORD_1 src1_sel:DWORD
	v_and_b32_sdwa v68, v77, v38 dst_sel:DWORD dst_unused:UNUSED_PAD src0_sel:WORD_1 src1_sel:DWORD
	v_add3_u32 v69, v80, v69, s36
	v_add3_u32 v74, v78, v74, s36
	v_add3_u32 v68, v77, v68, s36
	v_add3_u32 v35, v79, v35, s36
	v_and_b32_e32 v69, 0xffff0000, v69
	v_and_b32_e32 v74, 0xffff0000, v74
	v_or_b32_sdwa v69, v69, v35 dst_sel:DWORD dst_unused:UNUSED_PAD src0_sel:DWORD src1_sel:WORD_1
	v_or_b32_sdwa v68, v74, v68 dst_sel:DWORD dst_unused:UNUSED_PAD src0_sel:DWORD src1_sel:WORD_1
	global_store_dwordx4 v[72:73], v[66:69], off
	ds_read_b32 v35, v50
	ds_read_b32 v74, v50 offset:516
	ds_read_b32 v75, v50 offset:1032
	ds_read_b32 v76, v50 offset:1548
	ds_read_b32 v77, v50 offset:2064
	ds_read_b32 v78, v50 offset:2580
	ds_read_b32 v79, v50 offset:3096
	ds_read_b32 v80, v50 offset:3612
	v_add_u32_e32 v66, s4, v49
	v_lshlrev_b32_e32 v67, 1, v66
	v_and_b32_e32 v67, 0xffffffe0, v67
	v_add3_u32 v67, s1, v51, v67
	v_cndmask_b32_e32 v66, v67, v66, vcc
	v_ashrrev_i32_e32 v69, 31, v66
	v_mad_u64_u32 v[66:67], s[2:3], v66, s30, 0
	v_mov_b32_e32 v68, v67
	v_mad_u64_u32 v[68:69], s[2:3], v69, s30, v[68:69]
	v_mov_b32_e32 v67, v68
	v_lshl_add_u64 v[72:73], v[66:67], 1, v[70:71]
	s_waitcnt lgkmcnt(7)
	v_and_b32_sdwa v67, v35, v38 dst_sel:DWORD dst_unused:UNUSED_PAD src0_sel:WORD_1 src1_sel:DWORD
	v_add3_u32 v35, v35, v67, s36
	s_waitcnt lgkmcnt(4)
	v_and_b32_sdwa v67, v76, v38 dst_sel:DWORD dst_unused:UNUSED_PAD src0_sel:WORD_1 src1_sel:DWORD
	v_and_b32_sdwa v68, v74, v38 dst_sel:DWORD dst_unused:UNUSED_PAD src0_sel:WORD_1 src1_sel:DWORD
	v_and_b32_sdwa v66, v75, v38 dst_sel:DWORD dst_unused:UNUSED_PAD src0_sel:WORD_1 src1_sel:DWORD
	v_add3_u32 v67, v76, v67, s36
	v_add3_u32 v68, v74, v68, s36
	v_add3_u32 v66, v75, v66, s36
	v_and_b32_e32 v67, 0xffff0000, v67
	v_and_b32_e32 v68, 0xffff0000, v68
	s_waitcnt lgkmcnt(0)
	v_and_b32_sdwa v69, v80, v38 dst_sel:DWORD dst_unused:UNUSED_PAD src0_sel:WORD_1 src1_sel:DWORD
	v_and_b32_sdwa v74, v78, v38 dst_sel:DWORD dst_unused:UNUSED_PAD src0_sel:WORD_1 src1_sel:DWORD
	v_or_b32_sdwa v67, v67, v66 dst_sel:DWORD dst_unused:UNUSED_PAD src0_sel:DWORD src1_sel:WORD_1
	v_or_b32_sdwa v66, v68, v35 dst_sel:DWORD dst_unused:UNUSED_PAD src0_sel:DWORD src1_sel:WORD_1
	v_and_b32_sdwa v35, v79, v38 dst_sel:DWORD dst_unused:UNUSED_PAD src0_sel:WORD_1 src1_sel:DWORD
	v_and_b32_sdwa v68, v77, v38 dst_sel:DWORD dst_unused:UNUSED_PAD src0_sel:WORD_1 src1_sel:DWORD
	v_add3_u32 v69, v80, v69, s36
	v_add3_u32 v74, v78, v74, s36
	v_add3_u32 v68, v77, v68, s36
	v_add3_u32 v35, v79, v35, s36
	v_and_b32_e32 v69, 0xffff0000, v69
	v_and_b32_e32 v74, 0xffff0000, v74
	v_or_b32_sdwa v69, v69, v35 dst_sel:DWORD dst_unused:UNUSED_PAD src0_sel:DWORD src1_sel:WORD_1
	v_or_b32_sdwa v68, v74, v68 dst_sel:DWORD dst_unused:UNUSED_PAD src0_sel:DWORD src1_sel:WORD_1
	global_store_dwordx4 v[72:73], v[66:69], off
	ds_read_b32 v35, v53
	ds_read_b32 v74, v53 offset:516
	ds_read_b32 v75, v53 offset:1032
	ds_read_b32 v76, v53 offset:1548
	ds_read_b32 v77, v53 offset:2064
	ds_read_b32 v78, v53 offset:2580
	ds_read_b32 v79, v53 offset:3096
	ds_read_b32 v80, v53 offset:3612
	v_add_u32_e32 v66, s4, v52
	v_lshlrev_b32_e32 v67, 1, v66
	v_and_b32_e32 v67, 0xffffffe0, v67
	v_add3_u32 v67, s1, v54, v67
	v_cndmask_b32_e32 v66, v67, v66, vcc
	v_ashrrev_i32_e32 v69, 31, v66
	v_mad_u64_u32 v[66:67], s[2:3], v66, s30, 0
	v_mov_b32_e32 v68, v67
	v_mad_u64_u32 v[68:69], s[2:3], v69, s30, v[68:69]
	v_mov_b32_e32 v67, v68
	v_lshl_add_u64 v[72:73], v[66:67], 1, v[70:71]
	s_waitcnt lgkmcnt(7)
	v_and_b32_sdwa v67, v35, v38 dst_sel:DWORD dst_unused:UNUSED_PAD src0_sel:WORD_1 src1_sel:DWORD
	v_add3_u32 v35, v35, v67, s36
	s_waitcnt lgkmcnt(4)
	v_and_b32_sdwa v67, v76, v38 dst_sel:DWORD dst_unused:UNUSED_PAD src0_sel:WORD_1 src1_sel:DWORD
	v_and_b32_sdwa v68, v74, v38 dst_sel:DWORD dst_unused:UNUSED_PAD src0_sel:WORD_1 src1_sel:DWORD
	v_and_b32_sdwa v66, v75, v38 dst_sel:DWORD dst_unused:UNUSED_PAD src0_sel:WORD_1 src1_sel:DWORD
	v_add3_u32 v67, v76, v67, s36
	v_add3_u32 v68, v74, v68, s36
	v_add3_u32 v66, v75, v66, s36
	v_and_b32_e32 v67, 0xffff0000, v67
	v_and_b32_e32 v68, 0xffff0000, v68
	s_waitcnt lgkmcnt(0)
	v_and_b32_sdwa v69, v80, v38 dst_sel:DWORD dst_unused:UNUSED_PAD src0_sel:WORD_1 src1_sel:DWORD
	v_and_b32_sdwa v74, v78, v38 dst_sel:DWORD dst_unused:UNUSED_PAD src0_sel:WORD_1 src1_sel:DWORD
	v_or_b32_sdwa v67, v67, v66 dst_sel:DWORD dst_unused:UNUSED_PAD src0_sel:DWORD src1_sel:WORD_1
	v_or_b32_sdwa v66, v68, v35 dst_sel:DWORD dst_unused:UNUSED_PAD src0_sel:DWORD src1_sel:WORD_1
	v_and_b32_sdwa v35, v79, v38 dst_sel:DWORD dst_unused:UNUSED_PAD src0_sel:WORD_1 src1_sel:DWORD
	v_and_b32_sdwa v68, v77, v38 dst_sel:DWORD dst_unused:UNUSED_PAD src0_sel:WORD_1 src1_sel:DWORD
	v_add3_u32 v69, v80, v69, s36
	v_add3_u32 v74, v78, v74, s36
	v_add3_u32 v68, v77, v68, s36
	v_add3_u32 v35, v79, v35, s36
	v_and_b32_e32 v69, 0xffff0000, v69
	v_and_b32_e32 v74, 0xffff0000, v74
	v_or_b32_sdwa v69, v69, v35 dst_sel:DWORD dst_unused:UNUSED_PAD src0_sel:DWORD src1_sel:WORD_1
	v_or_b32_sdwa v68, v74, v68 dst_sel:DWORD dst_unused:UNUSED_PAD src0_sel:DWORD src1_sel:WORD_1
	global_store_dwordx4 v[72:73], v[66:69], off
	ds_read_b32 v35, v56
	ds_read_b32 v72, v56 offset:516
	ds_read_b32 v73, v56 offset:1032
	ds_read_b32 v74, v56 offset:1548
	ds_read_b32 v75, v56 offset:2064
	ds_read_b32 v76, v56 offset:2580
	ds_read_b32 v77, v56 offset:3096
	ds_read_b32 v78, v56 offset:3612
	v_add_u32_e32 v66, s4, v55
	v_lshlrev_b32_e32 v67, 1, v66
	v_and_b32_e32 v67, 0xffffffe0, v67
	v_add3_u32 v67, s1, v57, v67
	v_cndmask_b32_e32 v66, v67, v66, vcc
	v_ashrrev_i32_e32 v69, 31, v66
	v_mad_u64_u32 v[66:67], s[2:3], v66, s30, 0
	v_mov_b32_e32 v68, v67
	v_mad_u64_u32 v[68:69], s[2:3], v69, s30, v[68:69]
	v_mov_b32_e32 v67, v68
	v_lshl_add_u64 v[70:71], v[66:67], 1, v[70:71]
	s_waitcnt lgkmcnt(7)
	v_and_b32_sdwa v67, v35, v38 dst_sel:DWORD dst_unused:UNUSED_PAD src0_sel:WORD_1 src1_sel:DWORD
	v_add3_u32 v35, v35, v67, s36
	s_waitcnt lgkmcnt(4)
	v_and_b32_sdwa v67, v74, v38 dst_sel:DWORD dst_unused:UNUSED_PAD src0_sel:WORD_1 src1_sel:DWORD
	v_and_b32_sdwa v68, v72, v38 dst_sel:DWORD dst_unused:UNUSED_PAD src0_sel:WORD_1 src1_sel:DWORD
	v_and_b32_sdwa v66, v73, v38 dst_sel:DWORD dst_unused:UNUSED_PAD src0_sel:WORD_1 src1_sel:DWORD
	v_add3_u32 v67, v74, v67, s36
	v_add3_u32 v68, v72, v68, s36
	v_add3_u32 v66, v73, v66, s36
	v_and_b32_e32 v67, 0xffff0000, v67
	v_and_b32_e32 v68, 0xffff0000, v68
	s_waitcnt lgkmcnt(0)
	v_and_b32_sdwa v69, v78, v38 dst_sel:DWORD dst_unused:UNUSED_PAD src0_sel:WORD_1 src1_sel:DWORD
	v_and_b32_sdwa v72, v76, v38 dst_sel:DWORD dst_unused:UNUSED_PAD src0_sel:WORD_1 src1_sel:DWORD
	v_or_b32_sdwa v67, v67, v66 dst_sel:DWORD dst_unused:UNUSED_PAD src0_sel:DWORD src1_sel:WORD_1
	v_or_b32_sdwa v66, v68, v35 dst_sel:DWORD dst_unused:UNUSED_PAD src0_sel:DWORD src1_sel:WORD_1
	v_and_b32_sdwa v35, v77, v38 dst_sel:DWORD dst_unused:UNUSED_PAD src0_sel:WORD_1 src1_sel:DWORD
	v_and_b32_sdwa v68, v75, v38 dst_sel:DWORD dst_unused:UNUSED_PAD src0_sel:WORD_1 src1_sel:DWORD
	v_add3_u32 v69, v78, v69, s36
	v_add3_u32 v72, v76, v72, s36
	v_add3_u32 v68, v75, v68, s36
	v_add3_u32 v35, v77, v35, s36
	v_and_b32_e32 v69, 0xffff0000, v69
	v_and_b32_e32 v72, 0xffff0000, v72
	v_or_b32_sdwa v69, v69, v35 dst_sel:DWORD dst_unused:UNUSED_PAD src0_sel:DWORD src1_sel:WORD_1
	v_or_b32_sdwa v68, v72, v68 dst_sel:DWORD dst_unused:UNUSED_PAD src0_sel:DWORD src1_sel:WORD_1
	s_add_i32 s34, s34, 1
	s_and_b64 vcc, exec, s[20:21]
	s_mov_b32 s28, s37
	s_mov_b32 s1, s39
	s_mov_b32 s19, s6
	s_mov_b32 s4, s24
	s_mov_b32 s18, s29
	s_mov_b32 s30, s38
	s_mov_b64 s[2:3], s[22:23]
	global_store_dwordx4 v[70:71], v[66:69], off
	s_barrier
	s_cbranch_vccnz .LBB0_3818
